# accumulator zero-init removed: first MFMA of each accumulator in a unit takes inline 0 as C (trip-counter-selected copy of the first two MFMA clusters)
# baseline (speedup 1.0000x reference)
.LBB0_220:
	ds_read_b128 v[128:131], v172
	ds_read_b128 v[132:135], v172 offset:1024
	ds_read_b128 v[154:157], v172 offset:2048
	ds_read_b128 v[158:161], v172 offset:3072
	ds_read_b128 v[162:165], v173
	ds_read_b128 v[176:179], v173 offset:1024
	ds_read_b128 v[180:183], v173 offset:2048
	ds_read_b128 v[188:191], v173 offset:3072
	s_add_u32 s58, s56, 0x80
	s_addc_u32 s59, s57, 0
	s_cmp_eq_u32 s82, 12
	s_cselect_b32 s61, s9, s59
	s_cselect_b32 s60, s47, s58
	s_cselect_b32 s59, s45, s81
	s_cselect_b32 s58, s55, s80
	v_lshl_add_u64 v[166:167], s[56:57], 0, v[152:153]
	s_add_i32 m0, s69, 0xc000
	ds_read_b128 v[192:195], v174
	ds_read_b128 v[196:199], v174 offset:1024
	ds_read_b128 v[200:203], v174 offset:2048
	ds_read_b128 v[204:207], v174 offset:3072
	ds_read_b128 v[208:211], v174 offset:4096
	ds_read_b128 v[212:215], v174 offset:5120
	ds_read_b128 v[216:219], v174 offset:6144
	ds_read_b128 v[220:223], v174 offset:7168
	global_load_lds_dwordx4 v[166:167], off
	v_lshl_add_u64 v[166:167], s[56:57], 0, v[150:151]
	s_add_i32 m0, s69, 0xe000
	s_nop 0
	global_load_lds_dwordx4 v[166:167], off
	s_waitcnt vmcnt(8)
	s_waitcnt lgkmcnt(0)
	s_barrier
	s_setprio 1
	s_waitcnt lgkmcnt(0)
	s_cmp_eq_u32 s82, -2
	s_cbranch_scc1 .Lz_p2_f0
	v_mfma_f32_16x16x32_bf16 v[124:127], v[128:131], v[192:195], v[124:127]
	v_mfma_f32_16x16x32_bf16 v[120:123], v[154:157], v[192:195], v[120:123]
	v_mfma_f32_16x16x32_bf16 v[116:119], v[128:131], v[200:203], v[116:119]
	v_mfma_f32_16x16x32_bf16 v[112:115], v[154:157], v[200:203], v[112:115]
	v_mfma_f32_16x16x32_bf16 v[108:111], v[128:131], v[208:211], v[108:111]
	v_mfma_f32_16x16x32_bf16 v[104:107], v[154:157], v[208:211], v[104:107]
	v_mfma_f32_16x16x32_bf16 v[100:103], v[128:131], v[216:219], v[100:103]
	v_mfma_f32_16x16x32_bf16 v[96:99], v[154:157], v[216:219], v[96:99]
	v_mfma_f32_16x16x32_bf16 v[124:127], v[132:135], v[196:199], v[124:127]
	v_mfma_f32_16x16x32_bf16 v[120:123], v[158:161], v[196:199], v[120:123]
	v_mfma_f32_16x16x32_bf16 v[116:119], v[132:135], v[204:207], v[116:119]
	v_mfma_f32_16x16x32_bf16 v[112:115], v[158:161], v[204:207], v[112:115]
	v_mfma_f32_16x16x32_bf16 v[108:111], v[132:135], v[212:215], v[108:111]
	v_mfma_f32_16x16x32_bf16 v[104:107], v[158:161], v[212:215], v[104:107]
	v_mfma_f32_16x16x32_bf16 v[100:103], v[132:135], v[220:223], v[100:103]
	v_mfma_f32_16x16x32_bf16 v[96:99], v[158:161], v[220:223], v[96:99]
	s_setprio 0
	s_setprio 1
	v_mfma_f32_16x16x32_bf16 v[60:63], v[162:165], v[192:195], v[60:63]
	v_mfma_f32_16x16x32_bf16 v[56:59], v[180:183], v[192:195], v[56:59]
	v_mfma_f32_16x16x32_bf16 v[52:55], v[162:165], v[200:203], v[52:55]
	v_mfma_f32_16x16x32_bf16 v[48:51], v[180:183], v[200:203], v[48:51]
	v_mfma_f32_16x16x32_bf16 v[44:47], v[162:165], v[208:211], v[44:47]
	v_mfma_f32_16x16x32_bf16 v[40:43], v[180:183], v[208:211], v[40:43]
	v_mfma_f32_16x16x32_bf16 v[36:39], v[162:165], v[216:219], v[36:39]
	v_mfma_f32_16x16x32_bf16 v[32:35], v[180:183], v[216:219], v[32:35]
	v_mfma_f32_16x16x32_bf16 v[60:63], v[176:179], v[196:199], v[60:63]
	v_mfma_f32_16x16x32_bf16 v[56:59], v[188:191], v[196:199], v[56:59]
	v_mfma_f32_16x16x32_bf16 v[52:55], v[176:179], v[204:207], v[52:55]
	v_mfma_f32_16x16x32_bf16 v[48:51], v[188:191], v[204:207], v[48:51]
	v_mfma_f32_16x16x32_bf16 v[44:47], v[176:179], v[212:215], v[44:47]
	v_mfma_f32_16x16x32_bf16 v[40:43], v[188:191], v[212:215], v[40:43]
	v_mfma_f32_16x16x32_bf16 v[36:39], v[176:179], v[220:223], v[36:39]
	v_mfma_f32_16x16x32_bf16 v[32:35], v[188:191], v[220:223], v[32:35]
.Lz_p2_j0:
	s_setprio 0
	s_barrier
	s_add_i32 s83, s77, s68
	v_lshl_add_u64 v[166:167], s[58:59], 0, v[136:137]
	s_mov_b32 m0, s83
	ds_read_b128 v[192:195], v174 offset:16384
	ds_read_b128 v[196:199], v174 offset:17408
	ds_read_b128 v[200:203], v174 offset:18432
	ds_read_b128 v[204:207], v174 offset:19456
	ds_read_b128 v[208:211], v174 offset:20480
	ds_read_b128 v[212:215], v174 offset:21504
	ds_read_b128 v[216:219], v174 offset:22528
	ds_read_b128 v[220:223], v174 offset:23552
	global_load_lds_dwordx4 v[166:167], off
	s_add_i32 m0, s83, 0x2000
	s_add_u32 s84, s58, 0x40000
	v_lshl_add_u64 v[184:185], s[58:59], 0, v[142:143]
	s_addc_u32 s85, s59, 0
	s_add_i32 s83, s78, s68
	global_load_lds_dwordx4 v[184:185], off
	v_lshl_add_u64 v[224:225], s[84:85], 0, v[136:137]
	s_mov_b32 m0, s83
	v_lshl_add_u64 v[226:227], s[60:61], 0, v[144:145]
	global_load_lds_dwordx4 v[224:225], off
	v_lshl_add_u64 v[224:225], s[84:85], 0, v[142:143]
	s_add_i32 m0, s83, 0x2000
	s_nop 0
	global_load_lds_dwordx4 v[224:225], off
	v_lshl_add_u64 v[224:225], s[60:61], 0, v[138:139]
	s_mov_b32 m0, s69
	s_nop 0
	global_load_lds_dwordx4 v[224:225], off
	s_mov_b32 m0, s70
	s_nop 0
	global_load_lds_dwordx4 v[226:227], off
	s_waitcnt vmcnt(8)
	s_waitcnt lgkmcnt(0)
	s_barrier
	s_setprio 1
	s_waitcnt lgkmcnt(0)
	s_cmp_eq_u32 s82, -2
	s_cbranch_scc1 .Lz_p2_f1
	v_mfma_f32_16x16x32_bf16 v[92:95], v[128:131], v[192:195], v[92:95]
	v_mfma_f32_16x16x32_bf16 v[88:91], v[154:157], v[192:195], v[88:91]
	v_mfma_f32_16x16x32_bf16 v[84:87], v[128:131], v[200:203], v[84:87]
	v_mfma_f32_16x16x32_bf16 v[80:83], v[154:157], v[200:203], v[80:83]
	v_mfma_f32_16x16x32_bf16 v[76:79], v[128:131], v[208:211], v[76:79]
	v_mfma_f32_16x16x32_bf16 v[72:75], v[154:157], v[208:211], v[72:75]
	v_mfma_f32_16x16x32_bf16 v[68:71], v[128:131], v[216:219], v[68:71]
	v_mfma_f32_16x16x32_bf16 v[64:67], v[154:157], v[216:219], v[64:67]
	v_mfma_f32_16x16x32_bf16 v[92:95], v[132:135], v[196:199], v[92:95]
	v_mfma_f32_16x16x32_bf16 v[88:91], v[158:161], v[196:199], v[88:91]
	v_mfma_f32_16x16x32_bf16 v[84:87], v[132:135], v[204:207], v[84:87]
	v_mfma_f32_16x16x32_bf16 v[80:83], v[158:161], v[204:207], v[80:83]
	v_mfma_f32_16x16x32_bf16 v[76:79], v[132:135], v[212:215], v[76:79]
	v_mfma_f32_16x16x32_bf16 v[72:75], v[158:161], v[212:215], v[72:75]
	v_mfma_f32_16x16x32_bf16 v[68:71], v[132:135], v[220:223], v[68:71]
	v_mfma_f32_16x16x32_bf16 v[64:67], v[158:161], v[220:223], v[64:67]
	s_setprio 0
	s_setprio 1
	v_mfma_f32_16x16x32_bf16 v[28:31], v[162:165], v[192:195], v[28:31]
	v_mfma_f32_16x16x32_bf16 v[24:27], v[180:183], v[192:195], v[24:27]
	v_mfma_f32_16x16x32_bf16 v[20:23], v[162:165], v[200:203], v[20:23]
	v_mfma_f32_16x16x32_bf16 v[16:19], v[180:183], v[200:203], v[16:19]
	v_mfma_f32_16x16x32_bf16 v[12:15], v[162:165], v[208:211], v[12:15]
	v_mfma_f32_16x16x32_bf16 v[8:11], v[180:183], v[208:211], v[8:11]
	v_mfma_f32_16x16x32_bf16 v[4:7], v[162:165], v[216:219], v[4:7]
	v_mfma_f32_16x16x32_bf16 v[0:3], v[180:183], v[216:219], v[0:3]
	v_mfma_f32_16x16x32_bf16 v[28:31], v[176:179], v[196:199], v[28:31]
	v_mfma_f32_16x16x32_bf16 v[24:27], v[188:191], v[196:199], v[24:27]
	v_mfma_f32_16x16x32_bf16 v[20:23], v[176:179], v[204:207], v[20:23]
	v_mfma_f32_16x16x32_bf16 v[16:19], v[188:191], v[204:207], v[16:19]
	v_mfma_f32_16x16x32_bf16 v[12:15], v[176:179], v[212:215], v[12:15]
	v_mfma_f32_16x16x32_bf16 v[8:11], v[188:191], v[212:215], v[8:11]
	v_mfma_f32_16x16x32_bf16 v[4:7], v[176:179], v[220:223], v[4:7]
	v_mfma_f32_16x16x32_bf16 v[0:3], v[188:191], v[220:223], v[0:3]
.Lz_p2_j1:
	s_setprio 0
	s_barrier
	s_add_i32 s83, 0, 0x18000
	v_add_u32_e32 v148, s83, v169
	s_add_i32 s84, 0, 0x1c000
	ds_read_b128 v[128:131], v148
	ds_read_b128 v[132:135], v148 offset:1024
	ds_read_b128 v[154:157], v148 offset:2048
	ds_read_b128 v[158:161], v148 offset:3072
	v_add_u32_e32 v148, s84, v169
	ds_read_b128 v[162:165], v148
	ds_read_b128 v[176:179], v148 offset:1024
	ds_read_b128 v[180:183], v148 offset:2048
	ds_read_b128 v[188:191], v148 offset:3072
	s_mov_b32 m0, s71
	v_lshl_add_u64 v[228:229], s[60:61], 0, v[140:141]
	ds_read_b128 v[192:195], v174 offset:32768
	ds_read_b128 v[196:199], v174 offset:33792
	ds_read_b128 v[200:203], v174 offset:34816
	ds_read_b128 v[204:207], v174 offset:35840
	ds_read_b128 v[208:211], v174 offset:36864
	ds_read_b128 v[212:215], v174 offset:37888
	ds_read_b128 v[216:219], v174 offset:38912
	ds_read_b128 v[220:223], v174 offset:39936
	global_load_lds_dwordx4 v[228:229], off
	v_lshl_add_u64 v[228:229], s[60:61], 0, v[146:147]
	s_mov_b32 m0, s72
	s_nop 0
	global_load_lds_dwordx4 v[228:229], off
	s_waitcnt vmcnt(8)
	s_waitcnt lgkmcnt(0)
	s_barrier
	s_setprio 1
	s_waitcnt lgkmcnt(0)
	v_mfma_f32_16x16x32_bf16 v[124:127], v[128:131], v[192:195], v[124:127]
	v_mfma_f32_16x16x32_bf16 v[120:123], v[154:157], v[192:195], v[120:123]
	v_mfma_f32_16x16x32_bf16 v[116:119], v[128:131], v[200:203], v[116:119]
	v_mfma_f32_16x16x32_bf16 v[112:115], v[154:157], v[200:203], v[112:115]
	v_mfma_f32_16x16x32_bf16 v[108:111], v[128:131], v[208:211], v[108:111]
	v_mfma_f32_16x16x32_bf16 v[104:107], v[154:157], v[208:211], v[104:107]
	v_mfma_f32_16x16x32_bf16 v[100:103], v[128:131], v[216:219], v[100:103]
	v_mfma_f32_16x16x32_bf16 v[96:99], v[154:157], v[216:219], v[96:99]
	v_mfma_f32_16x16x32_bf16 v[124:127], v[132:135], v[196:199], v[124:127]
	v_mfma_f32_16x16x32_bf16 v[120:123], v[158:161], v[196:199], v[120:123]
	v_mfma_f32_16x16x32_bf16 v[116:119], v[132:135], v[204:207], v[116:119]
	v_mfma_f32_16x16x32_bf16 v[112:115], v[158:161], v[204:207], v[112:115]
	v_mfma_f32_16x16x32_bf16 v[108:111], v[132:135], v[212:215], v[108:111]
	v_mfma_f32_16x16x32_bf16 v[104:107], v[158:161], v[212:215], v[104:107]
	v_mfma_f32_16x16x32_bf16 v[100:103], v[132:135], v[220:223], v[100:103]
	v_mfma_f32_16x16x32_bf16 v[96:99], v[158:161], v[220:223], v[96:99]
	s_setprio 0
	s_setprio 1
	v_mfma_f32_16x16x32_bf16 v[60:63], v[162:165], v[192:195], v[60:63]
	v_mfma_f32_16x16x32_bf16 v[56:59], v[180:183], v[192:195], v[56:59]
	v_mfma_f32_16x16x32_bf16 v[52:55], v[162:165], v[200:203], v[52:55]
	v_mfma_f32_16x16x32_bf16 v[48:51], v[180:183], v[200:203], v[48:51]
	v_mfma_f32_16x16x32_bf16 v[44:47], v[162:165], v[208:211], v[44:47]
	v_mfma_f32_16x16x32_bf16 v[40:43], v[180:183], v[208:211], v[40:43]
	v_mfma_f32_16x16x32_bf16 v[36:39], v[162:165], v[216:219], v[36:39]
	v_mfma_f32_16x16x32_bf16 v[32:35], v[180:183], v[216:219], v[32:35]
	v_mfma_f32_16x16x32_bf16 v[60:63], v[176:179], v[196:199], v[60:63]
	v_mfma_f32_16x16x32_bf16 v[56:59], v[188:191], v[196:199], v[56:59]
	v_mfma_f32_16x16x32_bf16 v[52:55], v[176:179], v[204:207], v[52:55]
	v_mfma_f32_16x16x32_bf16 v[48:51], v[188:191], v[204:207], v[48:51]
	v_mfma_f32_16x16x32_bf16 v[44:47], v[176:179], v[212:215], v[44:47]
	v_mfma_f32_16x16x32_bf16 v[40:43], v[188:191], v[212:215], v[40:43]
	v_mfma_f32_16x16x32_bf16 v[36:39], v[176:179], v[220:223], v[36:39]
	v_mfma_f32_16x16x32_bf16 v[32:35], v[188:191], v[220:223], v[32:35]
	s_setprio 0
	s_barrier
	s_add_i32 s60, s83, s68
	v_lshl_add_u64 v[166:167], v[166:167], 0, s[18:19]
	s_mov_b32 m0, s60
	ds_read_b128 v[192:195], v174 offset:49152
	ds_read_b128 v[196:199], v174 offset:50176
	ds_read_b128 v[200:203], v174 offset:51200
	ds_read_b128 v[204:207], v174 offset:52224
	ds_read_b128 v[208:211], v174 offset:53248
	ds_read_b128 v[212:215], v174 offset:54272
	ds_read_b128 v[216:219], v174 offset:55296
	ds_read_b128 v[220:223], v174 offset:56320
	global_load_lds_dwordx4 v[166:167], off
	s_add_i32 m0, s60, 0x2000
	s_add_u32 s58, s58, 0x40080
	v_lshl_add_u64 v[166:167], v[184:185], 0, s[18:19]
	s_addc_u32 s59, s59, 0
	s_add_i32 s60, s84, s68
	global_load_lds_dwordx4 v[166:167], off
	v_lshl_add_u64 v[166:167], s[58:59], 0, v[136:137]
	s_mov_b32 m0, s60
	s_nop 0
	global_load_lds_dwordx4 v[166:167], off
	v_lshl_add_u64 v[166:167], s[58:59], 0, v[142:143]
	s_add_i32 m0, s60, 0x2000
	s_nop 0
	global_load_lds_dwordx4 v[166:167], off
	v_lshl_add_u64 v[166:167], v[224:225], 0, s[18:19]
	s_mov_b32 m0, s74
	s_nop 0
	global_load_lds_dwordx4 v[166:167], off
	v_lshl_add_u64 v[166:167], v[226:227], 0, s[18:19]
	s_mov_b32 m0, s75
	s_nop 0
	global_load_lds_dwordx4 v[166:167], off
	s_waitcnt vmcnt(8)
	s_waitcnt lgkmcnt(0)
	s_barrier
	s_setprio 1
	s_waitcnt lgkmcnt(0)
	v_mfma_f32_16x16x32_bf16 v[92:95], v[128:131], v[192:195], v[92:95]
	v_mfma_f32_16x16x32_bf16 v[88:91], v[154:157], v[192:195], v[88:91]
	v_mfma_f32_16x16x32_bf16 v[84:87], v[128:131], v[200:203], v[84:87]
	v_mfma_f32_16x16x32_bf16 v[80:83], v[154:157], v[200:203], v[80:83]
	v_mfma_f32_16x16x32_bf16 v[76:79], v[128:131], v[208:211], v[76:79]
	v_mfma_f32_16x16x32_bf16 v[72:75], v[154:157], v[208:211], v[72:75]
	v_mfma_f32_16x16x32_bf16 v[68:71], v[128:131], v[216:219], v[68:71]
	v_mfma_f32_16x16x32_bf16 v[64:67], v[154:157], v[216:219], v[64:67]
	v_mfma_f32_16x16x32_bf16 v[92:95], v[132:135], v[196:199], v[92:95]
	v_mfma_f32_16x16x32_bf16 v[88:91], v[158:161], v[196:199], v[88:91]
	v_mfma_f32_16x16x32_bf16 v[84:87], v[132:135], v[204:207], v[84:87]
	v_mfma_f32_16x16x32_bf16 v[80:83], v[158:161], v[204:207], v[80:83]
	v_mfma_f32_16x16x32_bf16 v[76:79], v[132:135], v[212:215], v[76:79]
	v_mfma_f32_16x16x32_bf16 v[72:75], v[158:161], v[212:215], v[72:75]
	v_mfma_f32_16x16x32_bf16 v[68:71], v[132:135], v[220:223], v[68:71]
	v_mfma_f32_16x16x32_bf16 v[64:67], v[158:161], v[220:223], v[64:67]
	s_setprio 0
	s_setprio 1
	v_mfma_f32_16x16x32_bf16 v[28:31], v[162:165], v[192:195], v[28:31]
	v_mfma_f32_16x16x32_bf16 v[24:27], v[180:183], v[192:195], v[24:27]
	v_mfma_f32_16x16x32_bf16 v[20:23], v[162:165], v[200:203], v[20:23]
	v_mfma_f32_16x16x32_bf16 v[16:19], v[180:183], v[200:203], v[16:19]
	v_mfma_f32_16x16x32_bf16 v[12:15], v[162:165], v[208:211], v[12:15]
	v_mfma_f32_16x16x32_bf16 v[8:11], v[180:183], v[208:211], v[8:11]
	v_mfma_f32_16x16x32_bf16 v[4:7], v[162:165], v[216:219], v[4:7]
	v_mfma_f32_16x16x32_bf16 v[0:3], v[180:183], v[216:219], v[0:3]
	v_mfma_f32_16x16x32_bf16 v[28:31], v[176:179], v[196:199], v[28:31]
	v_mfma_f32_16x16x32_bf16 v[24:27], v[188:191], v[196:199], v[24:27]
	v_mfma_f32_16x16x32_bf16 v[20:23], v[176:179], v[204:207], v[20:23]
	v_mfma_f32_16x16x32_bf16 v[16:19], v[188:191], v[204:207], v[16:19]
	v_mfma_f32_16x16x32_bf16 v[12:15], v[176:179], v[212:215], v[12:15]
	v_mfma_f32_16x16x32_bf16 v[8:11], v[188:191], v[212:215], v[8:11]
	v_mfma_f32_16x16x32_bf16 v[4:7], v[176:179], v[220:223], v[4:7]
	v_mfma_f32_16x16x32_bf16 v[0:3], v[188:191], v[220:223], v[0:3]
	s_setprio 0
	s_barrier
	s_add_i32 s82, s82, 2
	s_add_u32 s56, s56, 0x100
	s_addc_u32 s57, s57, 0
	s_add_u32 s80, s80, 0x100
	s_addc_u32 s81, s81, 0
	s_cmp_gt_u32 s82, 13
	s_cbranch_scc0 .LBB0_220
	s_branch .Lz_p2_exit
.Lz_p2_f0:
	v_mfma_f32_16x16x32_bf16 v[124:127], v[128:131], v[192:195], 0
	v_mfma_f32_16x16x32_bf16 v[120:123], v[154:157], v[192:195], 0
	v_mfma_f32_16x16x32_bf16 v[116:119], v[128:131], v[200:203], 0
	v_mfma_f32_16x16x32_bf16 v[112:115], v[154:157], v[200:203], 0
	v_mfma_f32_16x16x32_bf16 v[108:111], v[128:131], v[208:211], 0
	v_mfma_f32_16x16x32_bf16 v[104:107], v[154:157], v[208:211], 0
	v_mfma_f32_16x16x32_bf16 v[100:103], v[128:131], v[216:219], 0
	v_mfma_f32_16x16x32_bf16 v[96:99], v[154:157], v[216:219], 0
	v_mfma_f32_16x16x32_bf16 v[124:127], v[132:135], v[196:199], v[124:127]
	v_mfma_f32_16x16x32_bf16 v[120:123], v[158:161], v[196:199], v[120:123]
	v_mfma_f32_16x16x32_bf16 v[116:119], v[132:135], v[204:207], v[116:119]
	v_mfma_f32_16x16x32_bf16 v[112:115], v[158:161], v[204:207], v[112:115]
	v_mfma_f32_16x16x32_bf16 v[108:111], v[132:135], v[212:215], v[108:111]
	v_mfma_f32_16x16x32_bf16 v[104:107], v[158:161], v[212:215], v[104:107]
	v_mfma_f32_16x16x32_bf16 v[100:103], v[132:135], v[220:223], v[100:103]
	v_mfma_f32_16x16x32_bf16 v[96:99], v[158:161], v[220:223], v[96:99]
	s_setprio 0
	s_setprio 1
	v_mfma_f32_16x16x32_bf16 v[60:63], v[162:165], v[192:195], 0
	v_mfma_f32_16x16x32_bf16 v[56:59], v[180:183], v[192:195], 0
	v_mfma_f32_16x16x32_bf16 v[52:55], v[162:165], v[200:203], 0
	v_mfma_f32_16x16x32_bf16 v[48:51], v[180:183], v[200:203], 0
	v_mfma_f32_16x16x32_bf16 v[44:47], v[162:165], v[208:211], 0
	v_mfma_f32_16x16x32_bf16 v[40:43], v[180:183], v[208:211], 0
	v_mfma_f32_16x16x32_bf16 v[36:39], v[162:165], v[216:219], 0
	v_mfma_f32_16x16x32_bf16 v[32:35], v[180:183], v[216:219], 0
	v_mfma_f32_16x16x32_bf16 v[60:63], v[176:179], v[196:199], v[60:63]
	v_mfma_f32_16x16x32_bf16 v[56:59], v[188:191], v[196:199], v[56:59]
	v_mfma_f32_16x16x32_bf16 v[52:55], v[176:179], v[204:207], v[52:55]
	v_mfma_f32_16x16x32_bf16 v[48:51], v[188:191], v[204:207], v[48:51]
	v_mfma_f32_16x16x32_bf16 v[44:47], v[176:179], v[212:215], v[44:47]
	v_mfma_f32_16x16x32_bf16 v[40:43], v[188:191], v[212:215], v[40:43]
	v_mfma_f32_16x16x32_bf16 v[36:39], v[176:179], v[220:223], v[36:39]
	v_mfma_f32_16x16x32_bf16 v[32:35], v[188:191], v[220:223], v[32:35]
	s_branch .Lz_p2_j0
.Lz_p2_f1:
	v_mfma_f32_16x16x32_bf16 v[92:95], v[128:131], v[192:195], 0
	v_mfma_f32_16x16x32_bf16 v[88:91], v[154:157], v[192:195], 0
	v_mfma_f32_16x16x32_bf16 v[84:87], v[128:131], v[200:203], 0
	v_mfma_f32_16x16x32_bf16 v[80:83], v[154:157], v[200:203], 0
	v_mfma_f32_16x16x32_bf16 v[76:79], v[128:131], v[208:211], 0
	v_mfma_f32_16x16x32_bf16 v[72:75], v[154:157], v[208:211], 0
	v_mfma_f32_16x16x32_bf16 v[68:71], v[128:131], v[216:219], 0
	v_mfma_f32_16x16x32_bf16 v[64:67], v[154:157], v[216:219], 0
	v_mfma_f32_16x16x32_bf16 v[92:95], v[132:135], v[196:199], v[92:95]
	v_mfma_f32_16x16x32_bf16 v[88:91], v[158:161], v[196:199], v[88:91]
	v_mfma_f32_16x16x32_bf16 v[84:87], v[132:135], v[204:207], v[84:87]
	v_mfma_f32_16x16x32_bf16 v[80:83], v[158:161], v[204:207], v[80:83]
	v_mfma_f32_16x16x32_bf16 v[76:79], v[132:135], v[212:215], v[76:79]
	v_mfma_f32_16x16x32_bf16 v[72:75], v[158:161], v[212:215], v[72:75]
	v_mfma_f32_16x16x32_bf16 v[68:71], v[132:135], v[220:223], v[68:71]
	v_mfma_f32_16x16x32_bf16 v[64:67], v[158:161], v[220:223], v[64:67]
	s_setprio 0
	s_setprio 1
	v_mfma_f32_16x16x32_bf16 v[28:31], v[162:165], v[192:195], 0
	v_mfma_f32_16x16x32_bf16 v[24:27], v[180:183], v[192:195], 0
	v_mfma_f32_16x16x32_bf16 v[20:23], v[162:165], v[200:203], 0
	v_mfma_f32_16x16x32_bf16 v[16:19], v[180:183], v[200:203], 0
	v_mfma_f32_16x16x32_bf16 v[12:15], v[162:165], v[208:211], 0
	v_mfma_f32_16x16x32_bf16 v[8:11], v[180:183], v[208:211], 0
	v_mfma_f32_16x16x32_bf16 v[4:7], v[162:165], v[216:219], 0
	v_mfma_f32_16x16x32_bf16 v[0:3], v[180:183], v[216:219], 0
	v_mfma_f32_16x16x32_bf16 v[28:31], v[176:179], v[196:199], v[28:31]
	v_mfma_f32_16x16x32_bf16 v[24:27], v[188:191], v[196:199], v[24:27]
	v_mfma_f32_16x16x32_bf16 v[20:23], v[176:179], v[204:207], v[20:23]
	v_mfma_f32_16x16x32_bf16 v[16:19], v[188:191], v[204:207], v[16:19]
	v_mfma_f32_16x16x32_bf16 v[12:15], v[176:179], v[212:215], v[12:15]
	v_mfma_f32_16x16x32_bf16 v[8:11], v[188:191], v[212:215], v[8:11]
	v_mfma_f32_16x16x32_bf16 v[4:7], v[176:179], v[220:223], v[4:7]
	v_mfma_f32_16x16x32_bf16 v[0:3], v[188:191], v[220:223], v[0:3]
	s_branch .Lz_p2_j1
.Lz_p2_exit:
	s_and_b64 vcc, exec, s[20:21]
	s_cbranch_vccz .LBB0_223
	s_barrier

.LBB0_565:
	s_ashr_i32 s21, s20, 31
	s_lshl_b64 s[28:29], s[20:21], 19
	s_add_u32 s28, s33, s28
	s_addc_u32 s29, s42, s29
	s_and_b64 s[30:31], s[26:27], exec
	s_cselect_b32 s21, s29, s37
	s_cselect_b32 s56, s28, s36
	s_ashr_i32 s23, s22, 31
	s_lshl_b64 s[30:31], s[22:23], 19
	s_add_u32 s30, s43, s30
	s_addc_u32 s31, s44, s31
	s_and_b64 s[40:41], s[26:27], exec
	s_cselect_b32 s23, s31, s39
	s_cselect_b32 s57, s30, s38
	s_add_u32 s36, s36, 0x80
	s_addc_u32 s37, s37, 0
	s_add_u32 s58, s38, 0x100
	v_mov_b32_e32 v0, 0
	s_addc_u32 s59, s39, 0
	s_mov_b32 s60, -2
	s_waitcnt vmcnt(0)
.LBB0_566:
	ds_read_b128 v[128:131], v165
	ds_read_b128 v[132:135], v165 offset:1024
	ds_read_b128 v[152:155], v165 offset:2048
	ds_read_b128 v[156:159], v165 offset:3072
	ds_read_b128 v[168:171], v166
	ds_read_b128 v[172:175], v166 offset:1024
	ds_read_b128 v[176:179], v166 offset:2048
	ds_read_b128 v[180:183], v166 offset:3072
	s_add_u32 s38, s36, 0x80
	s_addc_u32 s39, s37, 0
	s_cmp_eq_u32 s60, 12
	s_cselect_b32 s41, s21, s39
	s_cselect_b32 s40, s56, s38
	s_cselect_b32 s39, s23, s59
	s_cselect_b32 s38, s57, s58
	v_lshl_add_u64 v[160:161], s[36:37], 0, v[150:151]
	s_add_i32 m0, s46, 0xc000
	ds_read_b128 v[188:191], v167
	ds_read_b128 v[192:195], v167 offset:1024
	ds_read_b128 v[196:199], v167 offset:2048
	ds_read_b128 v[200:203], v167 offset:3072
	ds_read_b128 v[204:207], v167 offset:4096
	ds_read_b128 v[208:211], v167 offset:5120
	ds_read_b128 v[212:215], v167 offset:6144
	ds_read_b128 v[216:219], v167 offset:7168
	global_load_lds_dwordx4 v[160:161], off
	v_lshl_add_u64 v[160:161], s[36:37], 0, v[148:149]
	s_add_i32 m0, s46, 0xe000
	s_nop 0
	global_load_lds_dwordx4 v[160:161], off
	s_waitcnt vmcnt(8)
	s_waitcnt lgkmcnt(0)
	s_barrier
	s_setprio 1
	s_waitcnt lgkmcnt(0)
	s_cmp_eq_u32 s60, -2
	s_cbranch_scc1 .Lz_p6_f0
	v_mfma_f32_16x16x32_bf16 v[124:127], v[128:131], v[188:191], v[124:127]
	v_mfma_f32_16x16x32_bf16 v[120:123], v[152:155], v[188:191], v[120:123]
	v_mfma_f32_16x16x32_bf16 v[116:119], v[128:131], v[196:199], v[116:119]
	v_mfma_f32_16x16x32_bf16 v[112:115], v[152:155], v[196:199], v[112:115]
	v_mfma_f32_16x16x32_bf16 v[108:111], v[128:131], v[204:207], v[108:111]
	v_mfma_f32_16x16x32_bf16 v[104:107], v[152:155], v[204:207], v[104:107]
	v_mfma_f32_16x16x32_bf16 v[100:103], v[128:131], v[212:215], v[100:103]
	v_mfma_f32_16x16x32_bf16 v[96:99], v[152:155], v[212:215], v[96:99]
	v_mfma_f32_16x16x32_bf16 v[124:127], v[132:135], v[192:195], v[124:127]
	v_mfma_f32_16x16x32_bf16 v[120:123], v[156:159], v[192:195], v[120:123]
	v_mfma_f32_16x16x32_bf16 v[116:119], v[132:135], v[200:203], v[116:119]
	v_mfma_f32_16x16x32_bf16 v[112:115], v[156:159], v[200:203], v[112:115]
	v_mfma_f32_16x16x32_bf16 v[108:111], v[132:135], v[208:211], v[108:111]
	v_mfma_f32_16x16x32_bf16 v[104:107], v[156:159], v[208:211], v[104:107]
	v_mfma_f32_16x16x32_bf16 v[100:103], v[132:135], v[216:219], v[100:103]
	v_mfma_f32_16x16x32_bf16 v[96:99], v[156:159], v[216:219], v[96:99]
	s_setprio 0
	s_setprio 1
	v_mfma_f32_16x16x32_bf16 v[68:71], v[168:171], v[188:191], v[68:71]
	v_mfma_f32_16x16x32_bf16 v[64:67], v[176:179], v[188:191], v[64:67]
	v_mfma_f32_16x16x32_bf16 v[52:55], v[168:171], v[196:199], v[52:55]
	v_mfma_f32_16x16x32_bf16 v[48:51], v[176:179], v[196:199], v[48:51]
	v_mfma_f32_16x16x32_bf16 v[44:47], v[168:171], v[204:207], v[44:47]
	v_mfma_f32_16x16x32_bf16 v[40:43], v[176:179], v[204:207], v[40:43]
	v_mfma_f32_16x16x32_bf16 v[36:39], v[168:171], v[212:215], v[36:39]
	v_mfma_f32_16x16x32_bf16 v[32:35], v[176:179], v[212:215], v[32:35]
	v_mfma_f32_16x16x32_bf16 v[68:71], v[172:175], v[192:195], v[68:71]
	v_mfma_f32_16x16x32_bf16 v[64:67], v[180:183], v[192:195], v[64:67]
	v_mfma_f32_16x16x32_bf16 v[52:55], v[172:175], v[200:203], v[52:55]
	v_mfma_f32_16x16x32_bf16 v[48:51], v[180:183], v[200:203], v[48:51]
	v_mfma_f32_16x16x32_bf16 v[44:47], v[172:175], v[208:211], v[44:47]
	v_mfma_f32_16x16x32_bf16 v[40:43], v[180:183], v[208:211], v[40:43]
	v_mfma_f32_16x16x32_bf16 v[36:39], v[172:175], v[216:219], v[36:39]
	v_mfma_f32_16x16x32_bf16 v[32:35], v[180:183], v[216:219], v[32:35]
.Lz_p6_j0:
	s_setprio 0
	s_barrier
	s_add_i32 s61, s54, s45
	v_lshl_add_u64 v[160:161], s[38:39], 0, v[146:147]
	s_mov_b32 m0, s61
	ds_read_b128 v[188:191], v167 offset:16384
	ds_read_b128 v[192:195], v167 offset:17408
	ds_read_b128 v[196:199], v167 offset:18432
	ds_read_b128 v[200:203], v167 offset:19456
	ds_read_b128 v[204:207], v167 offset:20480
	ds_read_b128 v[208:211], v167 offset:21504
	ds_read_b128 v[212:215], v167 offset:22528
	ds_read_b128 v[216:219], v167 offset:23552
	global_load_lds_dwordx4 v[160:161], off
	s_add_i32 m0, s61, 0x2000
	s_add_u32 s62, s38, 0x40000
	v_lshl_add_u64 v[184:185], s[38:39], 0, v[140:141]
	s_addc_u32 s63, s39, 0
	s_add_i32 s61, s55, s45
	global_load_lds_dwordx4 v[184:185], off
	v_lshl_add_u64 v[220:221], s[62:63], 0, v[146:147]
	s_mov_b32 m0, s61
	v_lshl_add_u64 v[222:223], s[40:41], 0, v[136:137]
	global_load_lds_dwordx4 v[220:221], off
	v_lshl_add_u64 v[220:221], s[62:63], 0, v[140:141]
	s_add_i32 m0, s61, 0x2000
	s_nop 0
	global_load_lds_dwordx4 v[220:221], off
	v_lshl_add_u64 v[220:221], s[40:41], 0, v[142:143]
	s_mov_b32 m0, s46
	s_nop 0
	global_load_lds_dwordx4 v[220:221], off
	s_mov_b32 m0, s47
	s_nop 0
	global_load_lds_dwordx4 v[222:223], off
	s_waitcnt vmcnt(8)
	s_waitcnt lgkmcnt(0)
	s_barrier
	s_setprio 1
	s_waitcnt lgkmcnt(0)
	s_cmp_eq_u32 s60, -2
	s_cbranch_scc1 .Lz_p6_f1
	v_mfma_f32_16x16x32_bf16 v[92:95], v[128:131], v[188:191], v[92:95]
	v_mfma_f32_16x16x32_bf16 v[88:91], v[152:155], v[188:191], v[88:91]
	v_mfma_f32_16x16x32_bf16 v[84:87], v[128:131], v[196:199], v[84:87]
	v_mfma_f32_16x16x32_bf16 v[80:83], v[152:155], v[196:199], v[80:83]
	v_mfma_f32_16x16x32_bf16 v[76:79], v[128:131], v[204:207], v[76:79]
	v_mfma_f32_16x16x32_bf16 v[72:75], v[152:155], v[204:207], v[72:75]
	v_mfma_f32_16x16x32_bf16 v[60:63], v[128:131], v[212:215], v[60:63]
	v_mfma_f32_16x16x32_bf16 v[56:59], v[152:155], v[212:215], v[56:59]
	v_mfma_f32_16x16x32_bf16 v[92:95], v[132:135], v[192:195], v[92:95]
	v_mfma_f32_16x16x32_bf16 v[88:91], v[156:159], v[192:195], v[88:91]
	v_mfma_f32_16x16x32_bf16 v[84:87], v[132:135], v[200:203], v[84:87]
	v_mfma_f32_16x16x32_bf16 v[80:83], v[156:159], v[200:203], v[80:83]
	v_mfma_f32_16x16x32_bf16 v[76:79], v[132:135], v[208:211], v[76:79]
	v_mfma_f32_16x16x32_bf16 v[72:75], v[156:159], v[208:211], v[72:75]
	v_mfma_f32_16x16x32_bf16 v[60:63], v[132:135], v[216:219], v[60:63]
	v_mfma_f32_16x16x32_bf16 v[56:59], v[156:159], v[216:219], v[56:59]
	s_setprio 0
	s_setprio 1
	v_mfma_f32_16x16x32_bf16 v[28:31], v[168:171], v[188:191], v[28:31]
	v_mfma_f32_16x16x32_bf16 v[24:27], v[176:179], v[188:191], v[24:27]
	v_mfma_f32_16x16x32_bf16 v[20:23], v[168:171], v[196:199], v[20:23]
	v_mfma_f32_16x16x32_bf16 v[16:19], v[176:179], v[196:199], v[16:19]
	v_mfma_f32_16x16x32_bf16 v[12:15], v[168:171], v[204:207], v[12:15]
	v_mfma_f32_16x16x32_bf16 v[8:11], v[176:179], v[204:207], v[8:11]
	v_mfma_f32_16x16x32_bf16 v[4:7], v[168:171], v[212:215], v[4:7]
	v_mfma_f32_16x16x32_bf16 v[0:3], v[176:179], v[212:215], v[0:3]
	v_mfma_f32_16x16x32_bf16 v[28:31], v[172:175], v[192:195], v[28:31]
	v_mfma_f32_16x16x32_bf16 v[24:27], v[180:183], v[192:195], v[24:27]
	v_mfma_f32_16x16x32_bf16 v[20:23], v[172:175], v[200:203], v[20:23]
	v_mfma_f32_16x16x32_bf16 v[16:19], v[180:183], v[200:203], v[16:19]
	v_mfma_f32_16x16x32_bf16 v[12:15], v[172:175], v[208:211], v[12:15]
	v_mfma_f32_16x16x32_bf16 v[8:11], v[180:183], v[208:211], v[8:11]
	v_mfma_f32_16x16x32_bf16 v[4:7], v[172:175], v[216:219], v[4:7]
	v_mfma_f32_16x16x32_bf16 v[0:3], v[180:183], v[216:219], v[0:3]
.Lz_p6_j1:
	s_setprio 0
	s_barrier
	s_add_i32 s61, 0, 0x18000
	s_add_i32 s62, 0, 0x1c000
	v_add_u32_e32 v156, s61, v163
	v_add_u32_e32 v180, s62, v163
	ds_read_b128 v[128:131], v156
	ds_read_b128 v[132:135], v156 offset:1024
	ds_read_b128 v[152:155], v156 offset:2048
	ds_read_b128 v[156:159], v156 offset:3072
	ds_read_b128 v[168:171], v180
	ds_read_b128 v[172:175], v180 offset:1024
	ds_read_b128 v[176:179], v180 offset:2048
	ds_read_b128 v[180:183], v180 offset:3072
	s_mov_b32 m0, s48
	v_lshl_add_u64 v[224:225], s[40:41], 0, v[144:145]
	ds_read_b128 v[188:191], v167 offset:32768
	ds_read_b128 v[192:195], v167 offset:33792
	ds_read_b128 v[196:199], v167 offset:34816
	ds_read_b128 v[200:203], v167 offset:35840
	ds_read_b128 v[204:207], v167 offset:36864
	ds_read_b128 v[208:211], v167 offset:37888
	ds_read_b128 v[212:215], v167 offset:38912
	ds_read_b128 v[216:219], v167 offset:39936
	global_load_lds_dwordx4 v[224:225], off
	v_lshl_add_u64 v[224:225], s[40:41], 0, v[138:139]
	s_mov_b32 m0, s49
	s_nop 0
	global_load_lds_dwordx4 v[224:225], off
	s_waitcnt vmcnt(8)
	s_waitcnt lgkmcnt(0)
	s_barrier
	s_setprio 1
	s_waitcnt lgkmcnt(0)
	v_mfma_f32_16x16x32_bf16 v[124:127], v[128:131], v[188:191], v[124:127]
	v_mfma_f32_16x16x32_bf16 v[120:123], v[152:155], v[188:191], v[120:123]
	v_mfma_f32_16x16x32_bf16 v[116:119], v[128:131], v[196:199], v[116:119]
	v_mfma_f32_16x16x32_bf16 v[112:115], v[152:155], v[196:199], v[112:115]
	v_mfma_f32_16x16x32_bf16 v[108:111], v[128:131], v[204:207], v[108:111]
	v_mfma_f32_16x16x32_bf16 v[104:107], v[152:155], v[204:207], v[104:107]
	v_mfma_f32_16x16x32_bf16 v[100:103], v[128:131], v[212:215], v[100:103]
	v_mfma_f32_16x16x32_bf16 v[96:99], v[152:155], v[212:215], v[96:99]
	v_mfma_f32_16x16x32_bf16 v[124:127], v[132:135], v[192:195], v[124:127]
	v_mfma_f32_16x16x32_bf16 v[120:123], v[156:159], v[192:195], v[120:123]
	v_mfma_f32_16x16x32_bf16 v[116:119], v[132:135], v[200:203], v[116:119]
	v_mfma_f32_16x16x32_bf16 v[112:115], v[156:159], v[200:203], v[112:115]
	v_mfma_f32_16x16x32_bf16 v[108:111], v[132:135], v[208:211], v[108:111]
	v_mfma_f32_16x16x32_bf16 v[104:107], v[156:159], v[208:211], v[104:107]
	v_mfma_f32_16x16x32_bf16 v[100:103], v[132:135], v[216:219], v[100:103]
	v_mfma_f32_16x16x32_bf16 v[96:99], v[156:159], v[216:219], v[96:99]
	s_setprio 0
	s_setprio 1
	v_mfma_f32_16x16x32_bf16 v[68:71], v[168:171], v[188:191], v[68:71]
	v_mfma_f32_16x16x32_bf16 v[64:67], v[176:179], v[188:191], v[64:67]
	v_mfma_f32_16x16x32_bf16 v[52:55], v[168:171], v[196:199], v[52:55]
	v_mfma_f32_16x16x32_bf16 v[48:51], v[176:179], v[196:199], v[48:51]
	v_mfma_f32_16x16x32_bf16 v[44:47], v[168:171], v[204:207], v[44:47]
	v_mfma_f32_16x16x32_bf16 v[40:43], v[176:179], v[204:207], v[40:43]
	v_mfma_f32_16x16x32_bf16 v[36:39], v[168:171], v[212:215], v[36:39]
	v_mfma_f32_16x16x32_bf16 v[32:35], v[176:179], v[212:215], v[32:35]
	v_mfma_f32_16x16x32_bf16 v[68:71], v[172:175], v[192:195], v[68:71]
	v_mfma_f32_16x16x32_bf16 v[64:67], v[180:183], v[192:195], v[64:67]
	v_mfma_f32_16x16x32_bf16 v[52:55], v[172:175], v[200:203], v[52:55]
	v_mfma_f32_16x16x32_bf16 v[48:51], v[180:183], v[200:203], v[48:51]
	v_mfma_f32_16x16x32_bf16 v[44:47], v[172:175], v[208:211], v[44:47]
	v_mfma_f32_16x16x32_bf16 v[40:43], v[180:183], v[208:211], v[40:43]
	v_mfma_f32_16x16x32_bf16 v[36:39], v[172:175], v[216:219], v[36:39]
	v_mfma_f32_16x16x32_bf16 v[32:35], v[180:183], v[216:219], v[32:35]
	s_setprio 0
	s_barrier
	s_add_i32 s40, s61, s45
	v_lshl_add_u64 v[160:161], v[160:161], 0, s[8:9]
	s_mov_b32 m0, s40
	ds_read_b128 v[188:191], v167 offset:49152
	ds_read_b128 v[192:195], v167 offset:50176
	ds_read_b128 v[196:199], v167 offset:51200
	ds_read_b128 v[200:203], v167 offset:52224
	ds_read_b128 v[204:207], v167 offset:53248
	ds_read_b128 v[208:211], v167 offset:54272
	ds_read_b128 v[212:215], v167 offset:55296
	ds_read_b128 v[216:219], v167 offset:56320
	global_load_lds_dwordx4 v[160:161], off
	s_add_i32 m0, s40, 0x2000
	s_add_u32 s38, s38, 0x40080
	v_lshl_add_u64 v[160:161], v[184:185], 0, s[8:9]
	s_addc_u32 s39, s39, 0
	s_add_i32 s40, s62, s45
	global_load_lds_dwordx4 v[160:161], off
	v_lshl_add_u64 v[160:161], s[38:39], 0, v[146:147]
	s_mov_b32 m0, s40
	s_nop 0
	global_load_lds_dwordx4 v[160:161], off
	v_lshl_add_u64 v[160:161], s[38:39], 0, v[140:141]
	s_add_i32 m0, s40, 0x2000
	s_nop 0
	global_load_lds_dwordx4 v[160:161], off
	v_lshl_add_u64 v[160:161], v[220:221], 0, s[8:9]
	s_mov_b32 m0, s51
	s_nop 0
	global_load_lds_dwordx4 v[160:161], off
	v_lshl_add_u64 v[160:161], v[222:223], 0, s[8:9]
	s_mov_b32 m0, s53
	s_nop 0
	global_load_lds_dwordx4 v[160:161], off
	s_waitcnt vmcnt(8)
	s_waitcnt lgkmcnt(0)
	s_barrier
	s_setprio 1
	s_waitcnt lgkmcnt(0)
	v_mfma_f32_16x16x32_bf16 v[92:95], v[128:131], v[188:191], v[92:95]
	v_mfma_f32_16x16x32_bf16 v[88:91], v[152:155], v[188:191], v[88:91]
	v_mfma_f32_16x16x32_bf16 v[84:87], v[128:131], v[196:199], v[84:87]
	v_mfma_f32_16x16x32_bf16 v[80:83], v[152:155], v[196:199], v[80:83]
	v_mfma_f32_16x16x32_bf16 v[76:79], v[128:131], v[204:207], v[76:79]
	v_mfma_f32_16x16x32_bf16 v[72:75], v[152:155], v[204:207], v[72:75]
	v_mfma_f32_16x16x32_bf16 v[60:63], v[128:131], v[212:215], v[60:63]
	v_mfma_f32_16x16x32_bf16 v[56:59], v[152:155], v[212:215], v[56:59]
	v_mfma_f32_16x16x32_bf16 v[92:95], v[132:135], v[192:195], v[92:95]
	v_mfma_f32_16x16x32_bf16 v[88:91], v[156:159], v[192:195], v[88:91]
	v_mfma_f32_16x16x32_bf16 v[84:87], v[132:135], v[200:203], v[84:87]
	v_mfma_f32_16x16x32_bf16 v[80:83], v[156:159], v[200:203], v[80:83]
	v_mfma_f32_16x16x32_bf16 v[76:79], v[132:135], v[208:211], v[76:79]
	v_mfma_f32_16x16x32_bf16 v[72:75], v[156:159], v[208:211], v[72:75]
	v_mfma_f32_16x16x32_bf16 v[60:63], v[132:135], v[216:219], v[60:63]
	v_mfma_f32_16x16x32_bf16 v[56:59], v[156:159], v[216:219], v[56:59]
	s_setprio 0
	s_setprio 1
	v_mfma_f32_16x16x32_bf16 v[28:31], v[168:171], v[188:191], v[28:31]
	v_mfma_f32_16x16x32_bf16 v[24:27], v[176:179], v[188:191], v[24:27]
	v_mfma_f32_16x16x32_bf16 v[20:23], v[168:171], v[196:199], v[20:23]
	v_mfma_f32_16x16x32_bf16 v[16:19], v[176:179], v[196:199], v[16:19]
	v_mfma_f32_16x16x32_bf16 v[12:15], v[168:171], v[204:207], v[12:15]
	v_mfma_f32_16x16x32_bf16 v[8:11], v[176:179], v[204:207], v[8:11]
	v_mfma_f32_16x16x32_bf16 v[4:7], v[168:171], v[212:215], v[4:7]
	v_mfma_f32_16x16x32_bf16 v[0:3], v[176:179], v[212:215], v[0:3]
	v_mfma_f32_16x16x32_bf16 v[28:31], v[172:175], v[192:195], v[28:31]
	v_mfma_f32_16x16x32_bf16 v[24:27], v[180:183], v[192:195], v[24:27]
	v_mfma_f32_16x16x32_bf16 v[20:23], v[172:175], v[200:203], v[20:23]
	v_mfma_f32_16x16x32_bf16 v[16:19], v[180:183], v[200:203], v[16:19]
	v_mfma_f32_16x16x32_bf16 v[12:15], v[172:175], v[208:211], v[12:15]
	v_mfma_f32_16x16x32_bf16 v[8:11], v[180:183], v[208:211], v[8:11]
	v_mfma_f32_16x16x32_bf16 v[4:7], v[172:175], v[216:219], v[4:7]
	v_mfma_f32_16x16x32_bf16 v[0:3], v[180:183], v[216:219], v[0:3]
	s_setprio 0
	s_barrier
	s_add_i32 s60, s60, 2
	s_add_u32 s36, s36, 0x100
	s_addc_u32 s37, s37, 0
	s_add_u32 s58, s58, 0x100
	s_addc_u32 s59, s59, 0
	s_cmp_gt_u32 s60, 13
	s_cbranch_scc0 .LBB0_566
	s_branch .Lz_p6_exit
.Lz_p6_f0:
	v_mfma_f32_16x16x32_bf16 v[124:127], v[128:131], v[188:191], 0
	v_mfma_f32_16x16x32_bf16 v[120:123], v[152:155], v[188:191], 0
	v_mfma_f32_16x16x32_bf16 v[116:119], v[128:131], v[196:199], 0
	v_mfma_f32_16x16x32_bf16 v[112:115], v[152:155], v[196:199], 0
	v_mfma_f32_16x16x32_bf16 v[108:111], v[128:131], v[204:207], 0
	v_mfma_f32_16x16x32_bf16 v[104:107], v[152:155], v[204:207], 0
	v_mfma_f32_16x16x32_bf16 v[100:103], v[128:131], v[212:215], 0
	v_mfma_f32_16x16x32_bf16 v[96:99], v[152:155], v[212:215], 0
	v_mfma_f32_16x16x32_bf16 v[124:127], v[132:135], v[192:195], v[124:127]
	v_mfma_f32_16x16x32_bf16 v[120:123], v[156:159], v[192:195], v[120:123]
	v_mfma_f32_16x16x32_bf16 v[116:119], v[132:135], v[200:203], v[116:119]
	v_mfma_f32_16x16x32_bf16 v[112:115], v[156:159], v[200:203], v[112:115]
	v_mfma_f32_16x16x32_bf16 v[108:111], v[132:135], v[208:211], v[108:111]
	v_mfma_f32_16x16x32_bf16 v[104:107], v[156:159], v[208:211], v[104:107]
	v_mfma_f32_16x16x32_bf16 v[100:103], v[132:135], v[216:219], v[100:103]
	v_mfma_f32_16x16x32_bf16 v[96:99], v[156:159], v[216:219], v[96:99]
	s_setprio 0
	s_setprio 1
	v_mfma_f32_16x16x32_bf16 v[68:71], v[168:171], v[188:191], 0
	v_mfma_f32_16x16x32_bf16 v[64:67], v[176:179], v[188:191], 0
	v_mfma_f32_16x16x32_bf16 v[52:55], v[168:171], v[196:199], 0
	v_mfma_f32_16x16x32_bf16 v[48:51], v[176:179], v[196:199], 0
	v_mfma_f32_16x16x32_bf16 v[44:47], v[168:171], v[204:207], 0
	v_mfma_f32_16x16x32_bf16 v[40:43], v[176:179], v[204:207], 0
	v_mfma_f32_16x16x32_bf16 v[36:39], v[168:171], v[212:215], 0
	v_mfma_f32_16x16x32_bf16 v[32:35], v[176:179], v[212:215], 0
	v_mfma_f32_16x16x32_bf16 v[68:71], v[172:175], v[192:195], v[68:71]
	v_mfma_f32_16x16x32_bf16 v[64:67], v[180:183], v[192:195], v[64:67]
	v_mfma_f32_16x16x32_bf16 v[52:55], v[172:175], v[200:203], v[52:55]
	v_mfma_f32_16x16x32_bf16 v[48:51], v[180:183], v[200:203], v[48:51]
	v_mfma_f32_16x16x32_bf16 v[44:47], v[172:175], v[208:211], v[44:47]
	v_mfma_f32_16x16x32_bf16 v[40:43], v[180:183], v[208:211], v[40:43]
	v_mfma_f32_16x16x32_bf16 v[36:39], v[172:175], v[216:219], v[36:39]
	v_mfma_f32_16x16x32_bf16 v[32:35], v[180:183], v[216:219], v[32:35]
	s_branch .Lz_p6_j0
.Lz_p6_f1:
	v_mfma_f32_16x16x32_bf16 v[92:95], v[128:131], v[188:191], 0
	v_mfma_f32_16x16x32_bf16 v[88:91], v[152:155], v[188:191], 0
	v_mfma_f32_16x16x32_bf16 v[84:87], v[128:131], v[196:199], 0
	v_mfma_f32_16x16x32_bf16 v[80:83], v[152:155], v[196:199], 0
	v_mfma_f32_16x16x32_bf16 v[76:79], v[128:131], v[204:207], 0
	v_mfma_f32_16x16x32_bf16 v[72:75], v[152:155], v[204:207], 0
	v_mfma_f32_16x16x32_bf16 v[60:63], v[128:131], v[212:215], 0
	v_mfma_f32_16x16x32_bf16 v[56:59], v[152:155], v[212:215], 0
	v_mfma_f32_16x16x32_bf16 v[92:95], v[132:135], v[192:195], v[92:95]
	v_mfma_f32_16x16x32_bf16 v[88:91], v[156:159], v[192:195], v[88:91]
	v_mfma_f32_16x16x32_bf16 v[84:87], v[132:135], v[200:203], v[84:87]
	v_mfma_f32_16x16x32_bf16 v[80:83], v[156:159], v[200:203], v[80:83]
	v_mfma_f32_16x16x32_bf16 v[76:79], v[132:135], v[208:211], v[76:79]
	v_mfma_f32_16x16x32_bf16 v[72:75], v[156:159], v[208:211], v[72:75]
	v_mfma_f32_16x16x32_bf16 v[60:63], v[132:135], v[216:219], v[60:63]
	v_mfma_f32_16x16x32_bf16 v[56:59], v[156:159], v[216:219], v[56:59]
	s_setprio 0
	s_setprio 1
	v_mfma_f32_16x16x32_bf16 v[28:31], v[168:171], v[188:191], 0
	v_mfma_f32_16x16x32_bf16 v[24:27], v[176:179], v[188:191], 0
	v_mfma_f32_16x16x32_bf16 v[20:23], v[168:171], v[196:199], 0
	v_mfma_f32_16x16x32_bf16 v[16:19], v[176:179], v[196:199], 0
	v_mfma_f32_16x16x32_bf16 v[12:15], v[168:171], v[204:207], 0
	v_mfma_f32_16x16x32_bf16 v[8:11], v[176:179], v[204:207], 0
	v_mfma_f32_16x16x32_bf16 v[4:7], v[168:171], v[212:215], 0
	v_mfma_f32_16x16x32_bf16 v[0:3], v[176:179], v[212:215], 0
	v_mfma_f32_16x16x32_bf16 v[28:31], v[172:175], v[192:195], v[28:31]
	v_mfma_f32_16x16x32_bf16 v[24:27], v[180:183], v[192:195], v[24:27]
	v_mfma_f32_16x16x32_bf16 v[20:23], v[172:175], v[200:203], v[20:23]
	v_mfma_f32_16x16x32_bf16 v[16:19], v[180:183], v[200:203], v[16:19]
	v_mfma_f32_16x16x32_bf16 v[12:15], v[172:175], v[208:211], v[12:15]
	v_mfma_f32_16x16x32_bf16 v[8:11], v[180:183], v[208:211], v[8:11]
	v_mfma_f32_16x16x32_bf16 v[4:7], v[172:175], v[216:219], v[4:7]
	v_mfma_f32_16x16x32_bf16 v[0:3], v[180:183], v[216:219], v[0:3]
	s_branch .Lz_p6_j1
.Lz_p6_exit:
	s_and_b64 vcc, exec, s[10:11]
	s_cbranch_vccz .LBB0_569
	s_barrier

.LBB0_1040:
	ds_read_b128 v[16:19], v191
	ds_read_b128 v[20:23], v191 offset:1024
	ds_read_b128 v[24:27], v191 offset:2048
	ds_read_b128 v[28:31], v191 offset:3072
	ds_read_b128 v[0:3], v192
	ds_read_b128 v[4:7], v192 offset:1024
	ds_read_b128 v[8:11], v192 offset:2048
	ds_read_b128 v[12:15], v192 offset:3072
	s_add_u32 s36, s34, 0x80
	s_addc_u32 s37, s35, 0
	s_cmp_eq_u32 s59, 4
	s_cselect_b32 s39, s15, s37
	s_cselect_b32 s38, s55, s36
	s_cselect_b32 s37, s13, s58
	s_cselect_b32 s36, s56, s57
	v_lshl_add_u64 v[220:221], s[34:35], 0, v[174:175]
	s_add_i32 m0, s27, 0xc000
	ds_read_b128 v[176:179], v193
	ds_read_b128 v[180:183], v193 offset:1024
	ds_read_b128 v[196:199], v193 offset:2048
	ds_read_b128 v[200:203], v193 offset:3072
	ds_read_b128 v[204:207], v193 offset:4096
	ds_read_b128 v[208:211], v193 offset:5120
	ds_read_b128 v[212:215], v193 offset:6144
	ds_read_b128 v[216:219], v193 offset:7168
	global_load_lds_dwordx4 v[220:221], off
	v_lshl_add_u64 v[220:221], s[34:35], 0, v[172:173]
	s_add_i32 m0, s27, 0xe000
	s_nop 0
	global_load_lds_dwordx4 v[220:221], off
	s_waitcnt vmcnt(8)
	s_waitcnt lgkmcnt(0)
	s_barrier
	s_setprio 1
	s_waitcnt lgkmcnt(0)
	s_cmp_eq_u32 s59, -2
	s_cbranch_scc1 .Lz_p9_f0
	v_mfma_scale_f32_16x16x128_f8f6f4 v[156:159], v[16:23], v[176:183], v[156:159], v184, v185 op_sel_hi:[0,0,0]
	v_mfma_scale_f32_16x16x128_f8f6f4 v[148:151], v[24:31], v[176:183], v[148:151], v184, v185 op_sel_hi:[0,0,0]
	v_mfma_scale_f32_16x16x128_f8f6f4 v[140:143], v[16:23], v[196:203], v[140:143], v184, v185 op_sel_hi:[0,0,0]
	v_mfma_scale_f32_16x16x128_f8f6f4 v[132:135], v[24:31], v[196:203], v[132:135], v184, v185 op_sel_hi:[0,0,0]
	v_mfma_scale_f32_16x16x128_f8f6f4 v[124:127], v[16:23], v[204:211], v[124:127], v184, v185 op_sel_hi:[0,0,0]
	v_mfma_scale_f32_16x16x128_f8f6f4 v[116:119], v[24:31], v[204:211], v[116:119], v184, v185 op_sel_hi:[0,0,0]
	v_mfma_scale_f32_16x16x128_f8f6f4 v[108:111], v[16:23], v[212:219], v[108:111], v184, v185 op_sel_hi:[0,0,0]
	v_mfma_scale_f32_16x16x128_f8f6f4 v[100:103], v[24:31], v[212:219], v[100:103], v184, v185 op_sel_hi:[0,0,0]
	s_setprio 0
	s_setprio 1
	v_mfma_scale_f32_16x16x128_f8f6f4 v[152:155], v[0:7], v[176:183], v[152:155], v184, v185 op_sel_hi:[0,0,0]
	v_mfma_scale_f32_16x16x128_f8f6f4 v[144:147], v[8:15], v[176:183], v[144:147], v184, v185 op_sel_hi:[0,0,0]
	v_mfma_scale_f32_16x16x128_f8f6f4 v[136:139], v[0:7], v[196:203], v[136:139], v184, v185 op_sel_hi:[0,0,0]
	v_mfma_scale_f32_16x16x128_f8f6f4 v[128:131], v[8:15], v[196:203], v[128:131], v184, v185 op_sel_hi:[0,0,0]
	v_mfma_scale_f32_16x16x128_f8f6f4 v[120:123], v[0:7], v[204:211], v[120:123], v184, v185 op_sel_hi:[0,0,0]
	v_mfma_scale_f32_16x16x128_f8f6f4 v[112:115], v[8:15], v[204:211], v[112:115], v184, v185 op_sel_hi:[0,0,0]
	v_mfma_scale_f32_16x16x128_f8f6f4 v[104:107], v[0:7], v[212:219], v[104:107], v184, v185 op_sel_hi:[0,0,0]
	v_mfma_scale_f32_16x16x128_f8f6f4 v[96:99], v[8:15], v[212:219], v[96:99], v184, v185 op_sel_hi:[0,0,0]
.Lz_p9_j0:
	s_setprio 0
	s_barrier
	s_add_i32 s60, s50, s41
	v_lshl_add_u64 v[176:177], s[36:37], 0, v[170:171]
	s_mov_b32 m0, s60
	ds_read_b128 v[196:199], v193 offset:16384
	ds_read_b128 v[200:203], v193 offset:17408
	ds_read_b128 v[204:207], v193 offset:18432
	ds_read_b128 v[208:211], v193 offset:19456
	ds_read_b128 v[212:215], v193 offset:20480
	ds_read_b128 v[216:219], v193 offset:21504
	ds_read_b128 v[220:223], v193 offset:22528
	ds_read_b128 v[224:227], v193 offset:23552
	global_load_lds_dwordx4 v[176:177], off
	s_add_i32 m0, s60, 0x2000
	s_add_u32 s60, s36, 0x20000
	v_lshl_add_u64 v[178:179], s[36:37], 0, v[168:169]
	s_addc_u32 s61, s37, 0
	s_add_i32 s62, s51, s41
	global_load_lds_dwordx4 v[178:179], off
	v_lshl_add_u64 v[180:181], s[60:61], 0, v[170:171]
	s_mov_b32 m0, s62
	v_lshl_add_u64 v[182:183], s[38:39], 0, v[160:161]
	global_load_lds_dwordx4 v[180:181], off
	v_lshl_add_u64 v[180:181], s[60:61], 0, v[168:169]
	s_add_i32 m0, s62, 0x2000
	s_nop 0
	global_load_lds_dwordx4 v[180:181], off
	v_lshl_add_u64 v[180:181], s[38:39], 0, v[164:165]
	s_mov_b32 m0, s27
	s_nop 0
	global_load_lds_dwordx4 v[180:181], off
	s_mov_b32 m0, s42
	s_nop 0
	global_load_lds_dwordx4 v[182:183], off
	s_waitcnt vmcnt(8)
	s_waitcnt lgkmcnt(0)
	s_barrier
	s_setprio 1
	s_waitcnt lgkmcnt(0)
	s_cmp_eq_u32 s59, -2
	s_cbranch_scc1 .Lz_p9_f1
	v_mfma_scale_f32_16x16x128_f8f6f4 v[92:95], v[16:23], v[196:203], v[92:95], v184, v185 op_sel_hi:[0,0,0]
	v_mfma_scale_f32_16x16x128_f8f6f4 v[84:87], v[24:31], v[196:203], v[84:87], v184, v185 op_sel_hi:[0,0,0]
	v_mfma_scale_f32_16x16x128_f8f6f4 v[76:79], v[16:23], v[204:211], v[76:79], v184, v185 op_sel_hi:[0,0,0]
	v_mfma_scale_f32_16x16x128_f8f6f4 v[68:71], v[24:31], v[204:211], v[68:71], v184, v185 op_sel_hi:[0,0,0]
	v_mfma_scale_f32_16x16x128_f8f6f4 v[60:63], v[16:23], v[212:219], v[60:63], v184, v185 op_sel_hi:[0,0,0]
	v_mfma_scale_f32_16x16x128_f8f6f4 v[52:55], v[24:31], v[212:219], v[52:55], v184, v185 op_sel_hi:[0,0,0]
	v_mfma_scale_f32_16x16x128_f8f6f4 v[44:47], v[16:23], v[220:227], v[44:47], v184, v185 op_sel_hi:[0,0,0]
	v_mfma_scale_f32_16x16x128_f8f6f4 v[36:39], v[24:31], v[220:227], v[36:39], v184, v185 op_sel_hi:[0,0,0]
	s_setprio 0
	s_setprio 1
	v_mfma_scale_f32_16x16x128_f8f6f4 v[88:91], v[0:7], v[196:203], v[88:91], v184, v185 op_sel_hi:[0,0,0]
	v_mfma_scale_f32_16x16x128_f8f6f4 v[80:83], v[8:15], v[196:203], v[80:83], v184, v185 op_sel_hi:[0,0,0]
	v_mfma_scale_f32_16x16x128_f8f6f4 v[72:75], v[0:7], v[204:211], v[72:75], v184, v185 op_sel_hi:[0,0,0]
	v_mfma_scale_f32_16x16x128_f8f6f4 v[64:67], v[8:15], v[204:211], v[64:67], v184, v185 op_sel_hi:[0,0,0]
	v_mfma_scale_f32_16x16x128_f8f6f4 v[56:59], v[0:7], v[212:219], v[56:59], v184, v185 op_sel_hi:[0,0,0]
	v_mfma_scale_f32_16x16x128_f8f6f4 v[48:51], v[8:15], v[212:219], v[48:51], v184, v185 op_sel_hi:[0,0,0]
	v_mfma_scale_f32_16x16x128_f8f6f4 v[40:43], v[0:7], v[220:227], v[40:43], v184, v185 op_sel_hi:[0,0,0]
	v_mfma_scale_f32_16x16x128_f8f6f4 v[32:35], v[8:15], v[220:227], v[32:35], v184, v185 op_sel_hi:[0,0,0]
.Lz_p9_j1:
	s_setprio 0
	s_barrier
	s_add_i32 s60, 0, 0x18000
	s_add_i32 s61, 0, 0x1c000
	v_add_u32_e32 v12, s60, v189
	v_add_u32_e32 v28, s61, v189
	ds_read_b128 v[0:3], v12
	ds_read_b128 v[4:7], v12 offset:1024
	ds_read_b128 v[8:11], v12 offset:2048
	ds_read_b128 v[12:15], v12 offset:3072
	ds_read_b128 v[16:19], v28
	ds_read_b128 v[20:23], v28 offset:1024
	ds_read_b128 v[24:27], v28 offset:2048
	ds_read_b128 v[28:31], v28 offset:3072
	s_mov_b32 m0, s43
	v_lshl_add_u64 v[228:229], s[38:39], 0, v[166:167]
	ds_read_b128 v[196:199], v193 offset:32768
	ds_read_b128 v[200:203], v193 offset:33792
	ds_read_b128 v[204:207], v193 offset:34816
	ds_read_b128 v[208:211], v193 offset:35840
	ds_read_b128 v[212:215], v193 offset:36864
	ds_read_b128 v[216:219], v193 offset:37888
	ds_read_b128 v[220:223], v193 offset:38912
	ds_read_b128 v[224:227], v193 offset:39936
	global_load_lds_dwordx4 v[228:229], off
	v_lshl_add_u64 v[228:229], s[38:39], 0, v[162:163]
	s_mov_b32 m0, s44
	s_nop 0
	global_load_lds_dwordx4 v[228:229], off
	s_waitcnt vmcnt(8)
	s_waitcnt lgkmcnt(0)
	s_barrier
	s_setprio 1
	s_waitcnt lgkmcnt(0)
	v_mfma_scale_f32_16x16x128_f8f6f4 v[156:159], v[0:7], v[196:203], v[156:159], v184, v185 op_sel_hi:[0,0,0]
	v_mfma_scale_f32_16x16x128_f8f6f4 v[148:151], v[8:15], v[196:203], v[148:151], v184, v185 op_sel_hi:[0,0,0]
	v_mfma_scale_f32_16x16x128_f8f6f4 v[140:143], v[0:7], v[204:211], v[140:143], v184, v185 op_sel_hi:[0,0,0]
	v_mfma_scale_f32_16x16x128_f8f6f4 v[132:135], v[8:15], v[204:211], v[132:135], v184, v185 op_sel_hi:[0,0,0]
	v_mfma_scale_f32_16x16x128_f8f6f4 v[124:127], v[0:7], v[212:219], v[124:127], v184, v185 op_sel_hi:[0,0,0]
	v_mfma_scale_f32_16x16x128_f8f6f4 v[116:119], v[8:15], v[212:219], v[116:119], v184, v185 op_sel_hi:[0,0,0]
	v_mfma_scale_f32_16x16x128_f8f6f4 v[108:111], v[0:7], v[220:227], v[108:111], v184, v185 op_sel_hi:[0,0,0]
	v_mfma_scale_f32_16x16x128_f8f6f4 v[100:103], v[8:15], v[220:227], v[100:103], v184, v185 op_sel_hi:[0,0,0]
	s_setprio 0
	s_setprio 1
	v_mfma_scale_f32_16x16x128_f8f6f4 v[152:155], v[16:23], v[196:203], v[152:155], v184, v185 op_sel_hi:[0,0,0]
	v_mfma_scale_f32_16x16x128_f8f6f4 v[144:147], v[24:31], v[196:203], v[144:147], v184, v185 op_sel_hi:[0,0,0]
	v_mfma_scale_f32_16x16x128_f8f6f4 v[136:139], v[16:23], v[204:211], v[136:139], v184, v185 op_sel_hi:[0,0,0]
	v_mfma_scale_f32_16x16x128_f8f6f4 v[128:131], v[24:31], v[204:211], v[128:131], v184, v185 op_sel_hi:[0,0,0]
	v_mfma_scale_f32_16x16x128_f8f6f4 v[120:123], v[16:23], v[212:219], v[120:123], v184, v185 op_sel_hi:[0,0,0]
	v_mfma_scale_f32_16x16x128_f8f6f4 v[112:115], v[24:31], v[212:219], v[112:115], v184, v185 op_sel_hi:[0,0,0]
	v_mfma_scale_f32_16x16x128_f8f6f4 v[104:107], v[16:23], v[220:227], v[104:107], v184, v185 op_sel_hi:[0,0,0]
	v_mfma_scale_f32_16x16x128_f8f6f4 v[96:99], v[24:31], v[220:227], v[96:99], v184, v185 op_sel_hi:[0,0,0]
	s_setprio 0
	s_barrier
	s_add_i32 s38, s60, s41
	v_lshl_add_u64 v[176:177], v[176:177], 0, s[4:5]
	s_mov_b32 m0, s38
	ds_read_b128 v[196:199], v193 offset:49152
	ds_read_b128 v[200:203], v193 offset:50176
	ds_read_b128 v[204:207], v193 offset:51200
	ds_read_b128 v[208:211], v193 offset:52224
	ds_read_b128 v[212:215], v193 offset:53248
	ds_read_b128 v[216:219], v193 offset:54272
	ds_read_b128 v[220:223], v193 offset:55296
	ds_read_b128 v[224:227], v193 offset:56320
	global_load_lds_dwordx4 v[176:177], off
	s_add_i32 m0, s38, 0x2000
	s_add_u32 s36, s36, 0x20080
	v_lshl_add_u64 v[176:177], v[178:179], 0, s[4:5]
	s_addc_u32 s37, s37, 0
	s_add_i32 s38, s61, s41
	global_load_lds_dwordx4 v[176:177], off
	v_lshl_add_u64 v[176:177], s[36:37], 0, v[170:171]
	s_mov_b32 m0, s38
	s_nop 0
	global_load_lds_dwordx4 v[176:177], off
	v_lshl_add_u64 v[176:177], s[36:37], 0, v[168:169]
	s_add_i32 m0, s38, 0x2000
	s_nop 0
	global_load_lds_dwordx4 v[176:177], off
	v_lshl_add_u64 v[176:177], v[180:181], 0, s[4:5]
	s_mov_b32 m0, s33
	s_nop 0
	global_load_lds_dwordx4 v[176:177], off
	v_lshl_add_u64 v[176:177], v[182:183], 0, s[4:5]
	s_mov_b32 m0, s48
	s_nop 0
	global_load_lds_dwordx4 v[176:177], off
	s_waitcnt vmcnt(8)
	s_waitcnt lgkmcnt(0)
	s_barrier
	s_setprio 1
	s_waitcnt lgkmcnt(0)
	v_mfma_scale_f32_16x16x128_f8f6f4 v[92:95], v[0:7], v[196:203], v[92:95], v184, v185 op_sel_hi:[0,0,0]
	v_mfma_scale_f32_16x16x128_f8f6f4 v[84:87], v[8:15], v[196:203], v[84:87], v184, v185 op_sel_hi:[0,0,0]
	v_mfma_scale_f32_16x16x128_f8f6f4 v[76:79], v[0:7], v[204:211], v[76:79], v184, v185 op_sel_hi:[0,0,0]
	v_mfma_scale_f32_16x16x128_f8f6f4 v[68:71], v[8:15], v[204:211], v[68:71], v184, v185 op_sel_hi:[0,0,0]
	v_mfma_scale_f32_16x16x128_f8f6f4 v[60:63], v[0:7], v[212:219], v[60:63], v184, v185 op_sel_hi:[0,0,0]
	v_mfma_scale_f32_16x16x128_f8f6f4 v[52:55], v[8:15], v[212:219], v[52:55], v184, v185 op_sel_hi:[0,0,0]
	v_mfma_scale_f32_16x16x128_f8f6f4 v[44:47], v[0:7], v[220:227], v[44:47], v184, v185 op_sel_hi:[0,0,0]
	v_mfma_scale_f32_16x16x128_f8f6f4 v[36:39], v[8:15], v[220:227], v[36:39], v184, v185 op_sel_hi:[0,0,0]
	s_setprio 0
	s_setprio 1
	v_mfma_scale_f32_16x16x128_f8f6f4 v[88:91], v[16:23], v[196:203], v[88:91], v184, v185 op_sel_hi:[0,0,0]
	v_mfma_scale_f32_16x16x128_f8f6f4 v[80:83], v[24:31], v[196:203], v[80:83], v184, v185 op_sel_hi:[0,0,0]
	v_mfma_scale_f32_16x16x128_f8f6f4 v[72:75], v[16:23], v[204:211], v[72:75], v184, v185 op_sel_hi:[0,0,0]
	v_mfma_scale_f32_16x16x128_f8f6f4 v[64:67], v[24:31], v[204:211], v[64:67], v184, v185 op_sel_hi:[0,0,0]
	v_mfma_scale_f32_16x16x128_f8f6f4 v[56:59], v[16:23], v[212:219], v[56:59], v184, v185 op_sel_hi:[0,0,0]
	v_mfma_scale_f32_16x16x128_f8f6f4 v[48:51], v[24:31], v[212:219], v[48:51], v184, v185 op_sel_hi:[0,0,0]
	v_mfma_scale_f32_16x16x128_f8f6f4 v[40:43], v[16:23], v[220:227], v[40:43], v184, v185 op_sel_hi:[0,0,0]
	v_mfma_scale_f32_16x16x128_f8f6f4 v[32:35], v[24:31], v[220:227], v[32:35], v184, v185 op_sel_hi:[0,0,0]
	s_setprio 0
	s_barrier
	s_add_i32 s59, s59, 2
	s_add_u32 s34, s34, 0x100
	s_addc_u32 s35, s35, 0
	s_add_u32 s57, s57, 0x100
	s_addc_u32 s58, s58, 0
	s_cmp_gt_u32 s59, 5
	s_cbranch_scc0 .LBB0_1040
	s_branch .Lz_p9_exit
.Lz_p9_f0:
	v_mfma_scale_f32_16x16x128_f8f6f4 v[156:159], v[16:23], v[176:183], 0, v184, v185 op_sel_hi:[0,0,0]
	v_mfma_scale_f32_16x16x128_f8f6f4 v[148:151], v[24:31], v[176:183], 0, v184, v185 op_sel_hi:[0,0,0]
	v_mfma_scale_f32_16x16x128_f8f6f4 v[140:143], v[16:23], v[196:203], 0, v184, v185 op_sel_hi:[0,0,0]
	v_mfma_scale_f32_16x16x128_f8f6f4 v[132:135], v[24:31], v[196:203], 0, v184, v185 op_sel_hi:[0,0,0]
	v_mfma_scale_f32_16x16x128_f8f6f4 v[124:127], v[16:23], v[204:211], 0, v184, v185 op_sel_hi:[0,0,0]
	v_mfma_scale_f32_16x16x128_f8f6f4 v[116:119], v[24:31], v[204:211], 0, v184, v185 op_sel_hi:[0,0,0]
	v_mfma_scale_f32_16x16x128_f8f6f4 v[108:111], v[16:23], v[212:219], 0, v184, v185 op_sel_hi:[0,0,0]
	v_mfma_scale_f32_16x16x128_f8f6f4 v[100:103], v[24:31], v[212:219], 0, v184, v185 op_sel_hi:[0,0,0]
	s_setprio 0
	s_setprio 1
	v_mfma_scale_f32_16x16x128_f8f6f4 v[152:155], v[0:7], v[176:183], 0, v184, v185 op_sel_hi:[0,0,0]
	v_mfma_scale_f32_16x16x128_f8f6f4 v[144:147], v[8:15], v[176:183], 0, v184, v185 op_sel_hi:[0,0,0]
	v_mfma_scale_f32_16x16x128_f8f6f4 v[136:139], v[0:7], v[196:203], 0, v184, v185 op_sel_hi:[0,0,0]
	v_mfma_scale_f32_16x16x128_f8f6f4 v[128:131], v[8:15], v[196:203], 0, v184, v185 op_sel_hi:[0,0,0]
	v_mfma_scale_f32_16x16x128_f8f6f4 v[120:123], v[0:7], v[204:211], 0, v184, v185 op_sel_hi:[0,0,0]
	v_mfma_scale_f32_16x16x128_f8f6f4 v[112:115], v[8:15], v[204:211], 0, v184, v185 op_sel_hi:[0,0,0]
	v_mfma_scale_f32_16x16x128_f8f6f4 v[104:107], v[0:7], v[212:219], 0, v184, v185 op_sel_hi:[0,0,0]
	v_mfma_scale_f32_16x16x128_f8f6f4 v[96:99], v[8:15], v[212:219], 0, v184, v185 op_sel_hi:[0,0,0]
	s_branch .Lz_p9_j0
.Lz_p9_f1:
	v_mfma_scale_f32_16x16x128_f8f6f4 v[92:95], v[16:23], v[196:203], 0, v184, v185 op_sel_hi:[0,0,0]
	v_mfma_scale_f32_16x16x128_f8f6f4 v[84:87], v[24:31], v[196:203], 0, v184, v185 op_sel_hi:[0,0,0]
	v_mfma_scale_f32_16x16x128_f8f6f4 v[76:79], v[16:23], v[204:211], 0, v184, v185 op_sel_hi:[0,0,0]
	v_mfma_scale_f32_16x16x128_f8f6f4 v[68:71], v[24:31], v[204:211], 0, v184, v185 op_sel_hi:[0,0,0]
	v_mfma_scale_f32_16x16x128_f8f6f4 v[60:63], v[16:23], v[212:219], 0, v184, v185 op_sel_hi:[0,0,0]
	v_mfma_scale_f32_16x16x128_f8f6f4 v[52:55], v[24:31], v[212:219], 0, v184, v185 op_sel_hi:[0,0,0]
	v_mfma_scale_f32_16x16x128_f8f6f4 v[44:47], v[16:23], v[220:227], 0, v184, v185 op_sel_hi:[0,0,0]
	v_mfma_scale_f32_16x16x128_f8f6f4 v[36:39], v[24:31], v[220:227], 0, v184, v185 op_sel_hi:[0,0,0]
	s_setprio 0
	s_setprio 1
	v_mfma_scale_f32_16x16x128_f8f6f4 v[88:91], v[0:7], v[196:203], 0, v184, v185 op_sel_hi:[0,0,0]
	v_mfma_scale_f32_16x16x128_f8f6f4 v[80:83], v[8:15], v[196:203], 0, v184, v185 op_sel_hi:[0,0,0]
	v_mfma_scale_f32_16x16x128_f8f6f4 v[72:75], v[0:7], v[204:211], 0, v184, v185 op_sel_hi:[0,0,0]
	v_mfma_scale_f32_16x16x128_f8f6f4 v[64:67], v[8:15], v[204:211], 0, v184, v185 op_sel_hi:[0,0,0]
	v_mfma_scale_f32_16x16x128_f8f6f4 v[56:59], v[0:7], v[212:219], 0, v184, v185 op_sel_hi:[0,0,0]
	v_mfma_scale_f32_16x16x128_f8f6f4 v[48:51], v[8:15], v[212:219], 0, v184, v185 op_sel_hi:[0,0,0]
	v_mfma_scale_f32_16x16x128_f8f6f4 v[40:43], v[0:7], v[220:227], 0, v184, v185 op_sel_hi:[0,0,0]
	v_mfma_scale_f32_16x16x128_f8f6f4 v[32:35], v[8:15], v[220:227], 0, v184, v185 op_sel_hi:[0,0,0]
	s_branch .Lz_p9_j1
.Lz_p9_exit:
	s_and_b64 vcc, exec, s[6:7]
	s_cbranch_vccz .LBB0_1043
	s_barrier

.LBB0_1181:
	ds_read_b128 v[16:19], v193
	ds_read_b128 v[20:23], v193 offset:1024
	ds_read_b128 v[24:27], v193 offset:2048
	ds_read_b128 v[28:31], v193 offset:3072
	ds_read_b128 v[0:3], v194
	ds_read_b128 v[4:7], v194 offset:1024
	ds_read_b128 v[8:11], v194 offset:2048
	ds_read_b128 v[12:15], v194 offset:3072
	s_add_u32 s0, s28, 0x100
	s_addc_u32 s1, s29, 0
	s_cmp_eq_u32 s62, 18
	s_cselect_b32 s35, s25, s1
	s_cselect_b32 s34, s24, s0
	s_cselect_b32 s31, s27, s61
	s_cselect_b32 s30, s26, s60
	s_mov_b32 m0, s50
	v_lshl_add_u64 v[222:223], s[28:29], 0, v[176:177]
	ds_read_b128 v[178:181], v195
	ds_read_b128 v[182:185], v195 offset:1024
	ds_read_b128 v[198:201], v195 offset:2048
	ds_read_b128 v[202:205], v195 offset:3072
	ds_read_b128 v[206:209], v195 offset:4096
	ds_read_b128 v[210:213], v195 offset:5120
	ds_read_b128 v[214:217], v195 offset:6144
	ds_read_b128 v[218:221], v195 offset:7168
	global_load_lds_dwordx4 v[222:223], off
	v_lshl_add_u64 v[222:223], s[28:29], 0, v[174:175]
	s_mov_b32 m0, s51
	s_nop 0
	global_load_lds_dwordx4 v[222:223], off
	s_waitcnt vmcnt(8)
	s_waitcnt lgkmcnt(0)
	s_barrier
	s_setprio 1
	s_waitcnt lgkmcnt(0)
	s_cmp_eq_u32 s62, -2
	s_cbranch_scc1 .Lz_p10_f0
	v_mfma_scale_f32_16x16x128_f8f6f4 v[156:159], v[16:23], v[178:185], v[156:159], v188, v189 op_sel_hi:[0,0,0]
	v_mfma_scale_f32_16x16x128_f8f6f4 v[152:155], v[24:31], v[178:185], v[152:155], v188, v189 op_sel_hi:[0,0,0]
	v_mfma_scale_f32_16x16x128_f8f6f4 v[140:143], v[16:23], v[198:205], v[140:143], v188, v189 op_sel_hi:[0,0,0]
	v_mfma_scale_f32_16x16x128_f8f6f4 v[136:139], v[24:31], v[198:205], v[136:139], v188, v189 op_sel_hi:[0,0,0]
	v_mfma_scale_f32_16x16x128_f8f6f4 v[124:127], v[16:23], v[206:213], v[124:127], v188, v189 op_sel_hi:[0,0,0]
	v_mfma_scale_f32_16x16x128_f8f6f4 v[120:123], v[24:31], v[206:213], v[120:123], v188, v189 op_sel_hi:[0,0,0]
	v_mfma_scale_f32_16x16x128_f8f6f4 v[108:111], v[16:23], v[214:221], v[108:111], v188, v189 op_sel_hi:[0,0,0]
	v_mfma_scale_f32_16x16x128_f8f6f4 v[104:107], v[24:31], v[214:221], v[104:107], v188, v189 op_sel_hi:[0,0,0]
	s_setprio 0
	s_setprio 1
	v_mfma_scale_f32_16x16x128_f8f6f4 v[148:151], v[0:7], v[178:185], v[148:151], v188, v189 op_sel_hi:[0,0,0]
	v_mfma_scale_f32_16x16x128_f8f6f4 v[144:147], v[8:15], v[178:185], v[144:147], v188, v189 op_sel_hi:[0,0,0]
	v_mfma_scale_f32_16x16x128_f8f6f4 v[132:135], v[0:7], v[198:205], v[132:135], v188, v189 op_sel_hi:[0,0,0]
	v_mfma_scale_f32_16x16x128_f8f6f4 v[128:131], v[8:15], v[198:205], v[128:131], v188, v189 op_sel_hi:[0,0,0]
	v_mfma_scale_f32_16x16x128_f8f6f4 v[116:119], v[0:7], v[206:213], v[116:119], v188, v189 op_sel_hi:[0,0,0]
	v_mfma_scale_f32_16x16x128_f8f6f4 v[112:115], v[8:15], v[206:213], v[112:115], v188, v189 op_sel_hi:[0,0,0]
	v_mfma_scale_f32_16x16x128_f8f6f4 v[100:103], v[0:7], v[214:221], v[100:103], v188, v189 op_sel_hi:[0,0,0]
	v_mfma_scale_f32_16x16x128_f8f6f4 v[96:99], v[8:15], v[214:221], v[96:99], v188, v189 op_sel_hi:[0,0,0]
.Lz_p10_j0:
	s_setprio 0
	s_barrier
	s_mov_b32 m0, s52
	v_lshl_add_u64 v[184:185], s[30:31], 0, v[170:171]
	s_add_u32 s28, s30, 0x58000
	ds_read_b128 v[198:201], v195 offset:16384
	ds_read_b128 v[202:205], v195 offset:17408
	ds_read_b128 v[206:209], v195 offset:18432
	ds_read_b128 v[210:213], v195 offset:19456
	ds_read_b128 v[214:217], v195 offset:20480
	ds_read_b128 v[218:221], v195 offset:21504
	ds_read_b128 v[222:225], v195 offset:22528
	ds_read_b128 v[226:229], v195 offset:23552
	global_load_lds_dwordx4 v[184:185], off
	v_lshl_add_u64 v[182:183], s[30:31], 0, v[168:169]
	s_mov_b32 m0, s53
	s_addc_u32 s29, s31, 0
	global_load_lds_dwordx4 v[182:183], off
	v_lshl_add_u64 v[178:179], s[28:29], 0, v[170:171]
	s_mov_b32 m0, s54
	v_lshl_add_u64 v[180:181], s[34:35], 0, v[160:161]
	global_load_lds_dwordx4 v[178:179], off
	v_lshl_add_u64 v[178:179], s[28:29], 0, v[168:169]
	s_mov_b32 m0, s55
	s_nop 0
	global_load_lds_dwordx4 v[178:179], off
	v_lshl_add_u64 v[178:179], s[34:35], 0, v[164:165]
	s_mov_b32 m0, s39
	s_nop 0
	global_load_lds_dwordx4 v[178:179], off
	s_mov_b32 m0, s40
	s_nop 0
	global_load_lds_dwordx4 v[180:181], off
	s_waitcnt vmcnt(8)
	s_waitcnt lgkmcnt(0)
	s_barrier
	s_setprio 1
	s_waitcnt lgkmcnt(0)
	s_cmp_eq_u32 s62, -2
	s_cbranch_scc1 .Lz_p10_f1
	v_mfma_scale_f32_16x16x128_f8f6f4 v[92:95], v[16:23], v[198:205], v[92:95], v188, v189 op_sel_hi:[0,0,0]
	v_mfma_scale_f32_16x16x128_f8f6f4 v[88:91], v[24:31], v[198:205], v[88:91], v188, v189 op_sel_hi:[0,0,0]
	v_mfma_scale_f32_16x16x128_f8f6f4 v[76:79], v[16:23], v[206:213], v[76:79], v188, v189 op_sel_hi:[0,0,0]
	v_mfma_scale_f32_16x16x128_f8f6f4 v[72:75], v[24:31], v[206:213], v[72:75], v188, v189 op_sel_hi:[0,0,0]
	v_mfma_scale_f32_16x16x128_f8f6f4 v[60:63], v[16:23], v[214:221], v[60:63], v188, v189 op_sel_hi:[0,0,0]
	v_mfma_scale_f32_16x16x128_f8f6f4 v[56:59], v[24:31], v[214:221], v[56:59], v188, v189 op_sel_hi:[0,0,0]
	v_mfma_scale_f32_16x16x128_f8f6f4 v[44:47], v[16:23], v[222:229], v[44:47], v188, v189 op_sel_hi:[0,0,0]
	v_mfma_scale_f32_16x16x128_f8f6f4 v[40:43], v[24:31], v[222:229], v[40:43], v188, v189 op_sel_hi:[0,0,0]
	s_setprio 0
	s_setprio 1
	v_mfma_scale_f32_16x16x128_f8f6f4 v[84:87], v[0:7], v[198:205], v[84:87], v188, v189 op_sel_hi:[0,0,0]
	v_mfma_scale_f32_16x16x128_f8f6f4 v[80:83], v[8:15], v[198:205], v[80:83], v188, v189 op_sel_hi:[0,0,0]
	v_mfma_scale_f32_16x16x128_f8f6f4 v[68:71], v[0:7], v[206:213], v[68:71], v188, v189 op_sel_hi:[0,0,0]
	v_mfma_scale_f32_16x16x128_f8f6f4 v[64:67], v[8:15], v[206:213], v[64:67], v188, v189 op_sel_hi:[0,0,0]
	v_mfma_scale_f32_16x16x128_f8f6f4 v[52:55], v[0:7], v[214:221], v[52:55], v188, v189 op_sel_hi:[0,0,0]
	v_mfma_scale_f32_16x16x128_f8f6f4 v[48:51], v[8:15], v[214:221], v[48:51], v188, v189 op_sel_hi:[0,0,0]
	v_mfma_scale_f32_16x16x128_f8f6f4 v[36:39], v[0:7], v[222:229], v[36:39], v188, v189 op_sel_hi:[0,0,0]
	v_mfma_scale_f32_16x16x128_f8f6f4 v[32:35], v[8:15], v[222:229], v[32:35], v188, v189 op_sel_hi:[0,0,0]
.Lz_p10_j1:
	s_setprio 0
	s_barrier
	s_add_i32 s63, 0, 0x1c000
	v_add_u32_e32 v28, s63, v191
	ds_read_b128 v[0:3], v196
	ds_read_b128 v[4:7], v196 offset:1024
	ds_read_b128 v[8:11], v196 offset:2048
	ds_read_b128 v[12:15], v196 offset:3072
	ds_read_b128 v[16:19], v28
	ds_read_b128 v[20:23], v28 offset:1024
	ds_read_b128 v[24:27], v28 offset:2048
	ds_read_b128 v[28:31], v28 offset:3072
	s_mov_b32 m0, s41
	v_lshl_add_u64 v[230:231], s[34:35], 0, v[166:167]
	ds_read_b128 v[198:201], v195 offset:32768
	ds_read_b128 v[202:205], v195 offset:33792
	ds_read_b128 v[206:209], v195 offset:34816
	ds_read_b128 v[210:213], v195 offset:35840
	ds_read_b128 v[214:217], v195 offset:36864
	ds_read_b128 v[218:221], v195 offset:37888
	ds_read_b128 v[222:225], v195 offset:38912
	ds_read_b128 v[226:229], v195 offset:39936
	global_load_lds_dwordx4 v[230:231], off
	v_lshl_add_u64 v[230:231], s[34:35], 0, v[162:163]
	s_mov_b32 m0, s42
	s_nop 0
	global_load_lds_dwordx4 v[230:231], off
	s_waitcnt vmcnt(8)
	s_waitcnt lgkmcnt(0)
	s_barrier
	s_setprio 1
	s_waitcnt lgkmcnt(0)
	v_mfma_scale_f32_16x16x128_f8f6f4 v[156:159], v[0:7], v[198:205], v[156:159], v188, v189 op_sel_hi:[0,0,0]
	v_mfma_scale_f32_16x16x128_f8f6f4 v[152:155], v[8:15], v[198:205], v[152:155], v188, v189 op_sel_hi:[0,0,0]
	v_mfma_scale_f32_16x16x128_f8f6f4 v[140:143], v[0:7], v[206:213], v[140:143], v188, v189 op_sel_hi:[0,0,0]
	v_mfma_scale_f32_16x16x128_f8f6f4 v[136:139], v[8:15], v[206:213], v[136:139], v188, v189 op_sel_hi:[0,0,0]
	v_mfma_scale_f32_16x16x128_f8f6f4 v[124:127], v[0:7], v[214:221], v[124:127], v188, v189 op_sel_hi:[0,0,0]
	v_mfma_scale_f32_16x16x128_f8f6f4 v[120:123], v[8:15], v[214:221], v[120:123], v188, v189 op_sel_hi:[0,0,0]
	v_mfma_scale_f32_16x16x128_f8f6f4 v[108:111], v[0:7], v[222:229], v[108:111], v188, v189 op_sel_hi:[0,0,0]
	v_mfma_scale_f32_16x16x128_f8f6f4 v[104:107], v[8:15], v[222:229], v[104:107], v188, v189 op_sel_hi:[0,0,0]
	s_setprio 0
	s_setprio 1
	v_mfma_scale_f32_16x16x128_f8f6f4 v[148:151], v[16:23], v[198:205], v[148:151], v188, v189 op_sel_hi:[0,0,0]
	v_mfma_scale_f32_16x16x128_f8f6f4 v[144:147], v[24:31], v[198:205], v[144:147], v188, v189 op_sel_hi:[0,0,0]
	v_mfma_scale_f32_16x16x128_f8f6f4 v[132:135], v[16:23], v[206:213], v[132:135], v188, v189 op_sel_hi:[0,0,0]
	v_mfma_scale_f32_16x16x128_f8f6f4 v[128:131], v[24:31], v[206:213], v[128:131], v188, v189 op_sel_hi:[0,0,0]
	v_mfma_scale_f32_16x16x128_f8f6f4 v[116:119], v[16:23], v[214:221], v[116:119], v188, v189 op_sel_hi:[0,0,0]
	v_mfma_scale_f32_16x16x128_f8f6f4 v[112:115], v[24:31], v[214:221], v[112:115], v188, v189 op_sel_hi:[0,0,0]
	v_mfma_scale_f32_16x16x128_f8f6f4 v[100:103], v[16:23], v[222:229], v[100:103], v188, v189 op_sel_hi:[0,0,0]
	v_mfma_scale_f32_16x16x128_f8f6f4 v[96:99], v[24:31], v[222:229], v[96:99], v188, v189 op_sel_hi:[0,0,0]
	s_setprio 0
	s_barrier
	s_add_i32 s28, s56, s38
	v_lshl_add_u64 v[184:185], v[184:185], 0, s[12:13]
	s_mov_b32 m0, s28
	ds_read_b128 v[198:201], v195 offset:49152
	ds_read_b128 v[202:205], v195 offset:50176
	ds_read_b128 v[206:209], v195 offset:51200
	ds_read_b128 v[210:213], v195 offset:52224
	ds_read_b128 v[214:217], v195 offset:53248
	ds_read_b128 v[218:221], v195 offset:54272
	ds_read_b128 v[222:225], v195 offset:55296
	ds_read_b128 v[226:229], v195 offset:56320
	global_load_lds_dwordx4 v[184:185], off
	s_add_i32 m0, s28, 0x2000
	s_add_u32 s28, s30, 0x58080
	v_lshl_add_u64 v[182:183], v[182:183], 0, s[12:13]
	s_addc_u32 s29, s31, 0
	s_add_i32 s30, s63, s38
	global_load_lds_dwordx4 v[182:183], off
	v_lshl_add_u64 v[182:183], s[28:29], 0, v[170:171]
	s_mov_b32 m0, s30
	v_lshl_add_u64 v[178:179], v[178:179], 0, s[12:13]
	global_load_lds_dwordx4 v[182:183], off
	v_lshl_add_u64 v[182:183], s[28:29], 0, v[168:169]
	s_add_i32 m0, s30, 0x2000
	s_nop 0
	global_load_lds_dwordx4 v[182:183], off
	s_mov_b32 m0, s45
	s_nop 0
	global_load_lds_dwordx4 v[178:179], off
	v_lshl_add_u64 v[178:179], v[180:181], 0, s[12:13]
	s_mov_b32 m0, s46
	s_nop 0
	global_load_lds_dwordx4 v[178:179], off
	s_waitcnt vmcnt(8)
	s_waitcnt lgkmcnt(0)
	s_barrier
	s_setprio 1
	s_waitcnt lgkmcnt(0)
	v_mfma_scale_f32_16x16x128_f8f6f4 v[92:95], v[0:7], v[198:205], v[92:95], v188, v189 op_sel_hi:[0,0,0]
	v_mfma_scale_f32_16x16x128_f8f6f4 v[88:91], v[8:15], v[198:205], v[88:91], v188, v189 op_sel_hi:[0,0,0]
	v_mfma_scale_f32_16x16x128_f8f6f4 v[76:79], v[0:7], v[206:213], v[76:79], v188, v189 op_sel_hi:[0,0,0]
	v_mfma_scale_f32_16x16x128_f8f6f4 v[72:75], v[8:15], v[206:213], v[72:75], v188, v189 op_sel_hi:[0,0,0]
	v_mfma_scale_f32_16x16x128_f8f6f4 v[60:63], v[0:7], v[214:221], v[60:63], v188, v189 op_sel_hi:[0,0,0]
	v_mfma_scale_f32_16x16x128_f8f6f4 v[56:59], v[8:15], v[214:221], v[56:59], v188, v189 op_sel_hi:[0,0,0]
	v_mfma_scale_f32_16x16x128_f8f6f4 v[44:47], v[0:7], v[222:229], v[44:47], v188, v189 op_sel_hi:[0,0,0]
	v_mfma_scale_f32_16x16x128_f8f6f4 v[40:43], v[8:15], v[222:229], v[40:43], v188, v189 op_sel_hi:[0,0,0]
	s_setprio 0
	s_setprio 1
	v_mfma_scale_f32_16x16x128_f8f6f4 v[84:87], v[16:23], v[198:205], v[84:87], v188, v189 op_sel_hi:[0,0,0]
	v_mfma_scale_f32_16x16x128_f8f6f4 v[80:83], v[24:31], v[198:205], v[80:83], v188, v189 op_sel_hi:[0,0,0]
	v_mfma_scale_f32_16x16x128_f8f6f4 v[68:71], v[16:23], v[206:213], v[68:71], v188, v189 op_sel_hi:[0,0,0]
	v_mfma_scale_f32_16x16x128_f8f6f4 v[64:67], v[24:31], v[206:213], v[64:67], v188, v189 op_sel_hi:[0,0,0]
	v_mfma_scale_f32_16x16x128_f8f6f4 v[52:55], v[16:23], v[214:221], v[52:55], v188, v189 op_sel_hi:[0,0,0]
	v_mfma_scale_f32_16x16x128_f8f6f4 v[48:51], v[24:31], v[214:221], v[48:51], v188, v189 op_sel_hi:[0,0,0]
	v_mfma_scale_f32_16x16x128_f8f6f4 v[36:39], v[16:23], v[222:229], v[36:39], v188, v189 op_sel_hi:[0,0,0]
	v_mfma_scale_f32_16x16x128_f8f6f4 v[32:35], v[24:31], v[222:229], v[32:35], v188, v189 op_sel_hi:[0,0,0]
	s_setprio 0
	s_barrier
	s_add_i32 s62, s62, 2
	s_add_u32 s60, s60, 0x100
	s_addc_u32 s61, s61, 0
	s_cmp_gt_u32 s62, 19
	s_mov_b64 s[28:29], s[0:1]
	s_cbranch_scc0 .LBB0_1181
	s_branch .Lz_p10_exit
.Lz_p10_f0:
	v_mfma_scale_f32_16x16x128_f8f6f4 v[156:159], v[16:23], v[178:185], 0, v188, v189 op_sel_hi:[0,0,0]
	v_mfma_scale_f32_16x16x128_f8f6f4 v[152:155], v[24:31], v[178:185], 0, v188, v189 op_sel_hi:[0,0,0]
	v_mfma_scale_f32_16x16x128_f8f6f4 v[140:143], v[16:23], v[198:205], 0, v188, v189 op_sel_hi:[0,0,0]
	v_mfma_scale_f32_16x16x128_f8f6f4 v[136:139], v[24:31], v[198:205], 0, v188, v189 op_sel_hi:[0,0,0]
	v_mfma_scale_f32_16x16x128_f8f6f4 v[124:127], v[16:23], v[206:213], 0, v188, v189 op_sel_hi:[0,0,0]
	v_mfma_scale_f32_16x16x128_f8f6f4 v[120:123], v[24:31], v[206:213], 0, v188, v189 op_sel_hi:[0,0,0]
	v_mfma_scale_f32_16x16x128_f8f6f4 v[108:111], v[16:23], v[214:221], 0, v188, v189 op_sel_hi:[0,0,0]
	v_mfma_scale_f32_16x16x128_f8f6f4 v[104:107], v[24:31], v[214:221], 0, v188, v189 op_sel_hi:[0,0,0]
	s_setprio 0
	s_setprio 1
	v_mfma_scale_f32_16x16x128_f8f6f4 v[148:151], v[0:7], v[178:185], 0, v188, v189 op_sel_hi:[0,0,0]
	v_mfma_scale_f32_16x16x128_f8f6f4 v[144:147], v[8:15], v[178:185], 0, v188, v189 op_sel_hi:[0,0,0]
	v_mfma_scale_f32_16x16x128_f8f6f4 v[132:135], v[0:7], v[198:205], 0, v188, v189 op_sel_hi:[0,0,0]
	v_mfma_scale_f32_16x16x128_f8f6f4 v[128:131], v[8:15], v[198:205], 0, v188, v189 op_sel_hi:[0,0,0]
	v_mfma_scale_f32_16x16x128_f8f6f4 v[116:119], v[0:7], v[206:213], 0, v188, v189 op_sel_hi:[0,0,0]
	v_mfma_scale_f32_16x16x128_f8f6f4 v[112:115], v[8:15], v[206:213], 0, v188, v189 op_sel_hi:[0,0,0]
	v_mfma_scale_f32_16x16x128_f8f6f4 v[100:103], v[0:7], v[214:221], 0, v188, v189 op_sel_hi:[0,0,0]
	v_mfma_scale_f32_16x16x128_f8f6f4 v[96:99], v[8:15], v[214:221], 0, v188, v189 op_sel_hi:[0,0,0]
	s_branch .Lz_p10_j0
.Lz_p10_f1:
	v_mfma_scale_f32_16x16x128_f8f6f4 v[92:95], v[16:23], v[198:205], 0, v188, v189 op_sel_hi:[0,0,0]
	v_mfma_scale_f32_16x16x128_f8f6f4 v[88:91], v[24:31], v[198:205], 0, v188, v189 op_sel_hi:[0,0,0]
	v_mfma_scale_f32_16x16x128_f8f6f4 v[76:79], v[16:23], v[206:213], 0, v188, v189 op_sel_hi:[0,0,0]
	v_mfma_scale_f32_16x16x128_f8f6f4 v[72:75], v[24:31], v[206:213], 0, v188, v189 op_sel_hi:[0,0,0]
	v_mfma_scale_f32_16x16x128_f8f6f4 v[60:63], v[16:23], v[214:221], 0, v188, v189 op_sel_hi:[0,0,0]
	v_mfma_scale_f32_16x16x128_f8f6f4 v[56:59], v[24:31], v[214:221], 0, v188, v189 op_sel_hi:[0,0,0]
	v_mfma_scale_f32_16x16x128_f8f6f4 v[44:47], v[16:23], v[222:229], 0, v188, v189 op_sel_hi:[0,0,0]
	v_mfma_scale_f32_16x16x128_f8f6f4 v[40:43], v[24:31], v[222:229], 0, v188, v189 op_sel_hi:[0,0,0]
	s_setprio 0
	s_setprio 1
	v_mfma_scale_f32_16x16x128_f8f6f4 v[84:87], v[0:7], v[198:205], 0, v188, v189 op_sel_hi:[0,0,0]
	v_mfma_scale_f32_16x16x128_f8f6f4 v[80:83], v[8:15], v[198:205], 0, v188, v189 op_sel_hi:[0,0,0]
	v_mfma_scale_f32_16x16x128_f8f6f4 v[68:71], v[0:7], v[206:213], 0, v188, v189 op_sel_hi:[0,0,0]
	v_mfma_scale_f32_16x16x128_f8f6f4 v[64:67], v[8:15], v[206:213], 0, v188, v189 op_sel_hi:[0,0,0]
	v_mfma_scale_f32_16x16x128_f8f6f4 v[52:55], v[0:7], v[214:221], 0, v188, v189 op_sel_hi:[0,0,0]
	v_mfma_scale_f32_16x16x128_f8f6f4 v[48:51], v[8:15], v[214:221], 0, v188, v189 op_sel_hi:[0,0,0]
	v_mfma_scale_f32_16x16x128_f8f6f4 v[36:39], v[0:7], v[222:229], 0, v188, v189 op_sel_hi:[0,0,0]
	v_mfma_scale_f32_16x16x128_f8f6f4 v[32:35], v[8:15], v[222:229], 0, v188, v189 op_sel_hi:[0,0,0]
	s_branch .Lz_p10_j1
.Lz_p10_exit:
	s_and_b64 vcc, exec, s[14:15]
	s_cbranch_vccz .LBB0_1184
	s_barrier
